# mLSTM pass 2: next chunk's K/Q prefetch loads land directly in the loop-carried registers (copies and the waits right after issue removed)
# baseline (speedup 1.0000x reference)
; #define LAS __attribute__((address_space(3)))
; template <bool PASS2, int DIRT>
; DI void mlstm_item(const Params& P, LAS unsigned char* lds, int st, int g) {
;     ...
;             { const int j = tid & 127, part = tid >> 7; float s = 0.f;
; #pragma unroll
;               for (int cc = 0; cc < 4; ++cc) { const u32x4 q8 = *(const LAS u32x4*)(QS + off_b(j, 4 * part + cc)); const f32x4 n0a = *(const LAS f32x4*)(sN0 + 32 * part + 8 * cc), n0b = *(const LAS f32x4*)(sN0 + 32 * part + 8 * cc + 4);
;                   s += bf_lo(q8.x) * n0a[0] + bf_hi(q8.x) * n0a[1] + bf_lo(q8.y) * n0a[2] + bf_hi(q8.y) * n0a[3] + bf_lo(q8.z) * n0b[0] + bf_hi(q8.z) * n0b[1] + bf_lo(q8.w) * n0b[2] + bf_hi(q8.w) * n0b[3]; }
;               sQNP[part * 128 + j] = s; }
;             tid = (wid << 6) | lane_id(); asm volatile("" : "+v"(tid)); lane = tid & 63; r = lane & 31; hh = lane >> 5;
; #pragma unroll
;             for (int jt = 0; jt < 4; ++jt)
; #pragma unroll
;                 for (int e = 0; e < 16; ++e) num[jt][e] = 0.f;
;             {
;                 bf16x8 qf[2][4];
;                 auto ldq = [&](int g_, bf16x8 (&qb)[4]) { const int dkt = g_ >> 1, s2 = g_ & 1;
; #pragma unroll
;                     for (int jt = 0; jt < 4; ++jt) { const s16x4 lo = *(const LAS s16x4*)(QS + off_b(32 * jt + r, 4 * dkt + 2 * s2) + 8 * hh); const s16x4 hi = *(const LAS s16x4*)(QS + off_b(32 * jt + r, 4 * dkt + 2 * s2 + 1) + 8 * hh);
;                         qb[jt] = __builtin_shufflevector(lo, hi, 0, 1, 2, 3, 4, 5, 6, 7); } };
;                 ldq(0, qf[0]);
; #pragma unroll
;                 for (int g_ = 0; g_ < 8; ++g_) { const int dkt = g_ >> 1, s2 = g_ & 1;
;                     if (g_ + 1 < 8) ldq(g_ + 1, qf[(g_ + 1) & 1]);
;                     __builtin_amdgcn_sched_barrier(0);
;                     u32x4 xp; xp.x = pk2(C[dkt][8 * s2 + 0], C[dkt][8 * s2 + 1]); xp.y = pk2(C[dkt][8 * s2 + 2], C[dkt][8 * s2 + 3]); xp.z = pk2(C[dkt][8 * s2 + 4], C[dkt][8 * s2 + 5]); xp.w = pk2(C[dkt][8 * s2 + 6], C[dkt][8 * s2 + 7]);
;                     const bf16x8 xs = __builtin_bit_cast(bf16x8, xp);
; #pragma unroll
;                     for (int jt = 0; jt < 4; ++jt) num[jt] = MFMA32(xs, qf[g_ & 1][jt], num[jt]);
;                     __builtin_amdgcn_sched_barrier(0);
;                     if (s2 == 1) asm volatile("" : "+v"(num[0]), "+v"(num[1]), "+v"(num[2]), "+v"(num[3]) :: "memory"); }
.LBB0_755:
	s_and_saveexec_b64 s[2:3], s[44:45]
	ds_write_b32 v86, v64 offset:128
	s_or_b64 exec, exec, s[2:3]
	v_and_b32_e32 v65, 0xffffff80, v80
	v_add_u32_e32 v65, 0, v65
	v_and_b32_e32 v64, 0x7f, v80
	v_add_u32_e32 v81, 0x1a600, v65
	v_ashrrev_i32_e32 v65, 1, v80
	v_mul_u32_u24_e32 v64, 0x110, v64
	v_and_b32_e32 v65, 0xffffffc0, v65
	v_add3_u32 v76, 0, v64, v65
	s_waitcnt lgkmcnt(1)
	ds_read_b128 v[64:67], v76
	ds_read_b128 v[68:71], v76 offset:16
	ds_read_b128 v[72:75], v76 offset:32
	ds_read_b128 v[76:79], v76 offset:48
	ds_read_b128 v[82:85], v81
	ds_read_b128 v[86:89], v81 offset:16
	ds_read_b128 v[90:93], v81 offset:32
	ds_read_b128 v[94:97], v81 offset:48
	s_waitcnt lgkmcnt(6)
	v_and_b32_e32 v103, 0xffff0000, v68
	v_and_b32_e32 v102, 0xffff0000, v64
	v_lshlrev_b32_e32 v99, 16, v68
	s_waitcnt lgkmcnt(1)
	v_mov_b32_e32 v101, v90
	v_mov_b32_e32 v90, v83
	v_lshlrev_b32_e32 v98, 16, v64
	v_mov_b32_e32 v100, v82
	v_pk_mul_f32 v[82:83], v[90:91], v[102:103]
	v_lshlrev_b32_e32 v91, 16, v69
	v_pk_fma_f32 v[82:83], v[100:101], v[98:99], v[82:83]
	v_lshlrev_b32_e32 v90, 16, v65
	v_mov_b32_e32 v98, v84
	v_mov_b32_e32 v99, v92
	v_pk_fma_f32 v[82:83], v[98:99], v[90:91], v[82:83]
	v_and_b32_e32 v69, 0xffff0000, v69
	v_and_b32_e32 v68, 0xffff0000, v65
	v_mov_b32_e32 v92, v85
	v_pk_fma_f32 v[64:65], v[92:93], v[68:69], v[82:83]
	v_lshlrev_b32_e32 v69, 16, v70
	v_lshlrev_b32_e32 v68, 16, v66
	v_mov_b32_e32 v82, v86
	s_waitcnt lgkmcnt(0)
	v_mov_b32_e32 v83, v94
	v_pk_fma_f32 v[64:65], v[82:83], v[68:69], v[64:65]
	v_and_b32_e32 v69, 0xffff0000, v70
	v_and_b32_e32 v68, 0xffff0000, v66
	v_mov_b32_e32 v94, v87
	v_pk_fma_f32 v[64:65], v[94:95], v[68:69], v[64:65]
	v_lshlrev_b32_e32 v69, 16, v71
	v_lshlrev_b32_e32 v68, 16, v67
	v_mov_b32_e32 v82, v88
	v_mov_b32_e32 v83, v96
	v_pk_fma_f32 v[64:65], v[82:83], v[68:69], v[64:65]
	v_and_b32_e32 v69, 0xffff0000, v71
	v_and_b32_e32 v68, 0xffff0000, v67
	v_mov_b32_e32 v96, v89
	v_pk_fma_f32 v[64:65], v[96:97], v[68:69], v[64:65]
	v_and_b32_e32 v95, 0xffff0000, v76
	v_add_f32_e32 v64, 0, v64
	v_add_f32_e32 v96, v64, v65
	ds_read_b128 v[64:67], v81 offset:64
	ds_read_b128 v[68:71], v81 offset:80
	ds_read_b128 v[82:85], v81 offset:96
	ds_read_b128 v[86:89], v81 offset:112
	v_and_b32_e32 v94, 0xffff0000, v72
	v_lshlrev_b32_e32 v91, 16, v76
	v_lshlrev_b32_e32 v90, 16, v72
	s_waitcnt lgkmcnt(1)
	v_mov_b32_e32 v93, v82
	v_mov_b32_e32 v82, v65
	v_mov_b32_e32 v92, v64
	v_pk_mul_f32 v[64:65], v[82:83], v[94:95]
	v_lshlrev_b32_e32 v83, 16, v77
	v_pk_fma_f32 v[64:65], v[92:93], v[90:91], v[64:65]
	v_lshlrev_b32_e32 v82, 16, v73
	v_mov_b32_e32 v90, v66
	v_mov_b32_e32 v91, v84
	v_pk_fma_f32 v[64:65], v[90:91], v[82:83], v[64:65]
	v_and_b32_e32 v77, 0xffff0000, v77
	v_and_b32_e32 v76, 0xffff0000, v73
	v_mov_b32_e32 v84, v67
	v_pk_fma_f32 v[64:65], v[84:85], v[76:77], v[64:65]
	v_lshlrev_b32_e32 v67, 16, v78
	v_lshlrev_b32_e32 v66, 16, v74
	v_mov_b32_e32 v72, v68
	s_waitcnt lgkmcnt(0)
	v_mov_b32_e32 v73, v86
	v_pk_fma_f32 v[64:65], v[72:73], v[66:67], v[64:65]
	v_and_b32_e32 v67, 0xffff0000, v78
	v_and_b32_e32 v66, 0xffff0000, v74
	v_mov_b32_e32 v86, v69
	v_pk_fma_f32 v[64:65], v[86:87], v[66:67], v[64:65]
	v_lshlrev_b32_e32 v67, 16, v79
	v_lshlrev_b32_e32 v66, 16, v75
	v_mov_b32_e32 v68, v70
	v_mov_b32_e32 v69, v88
	v_pk_fma_f32 v[64:65], v[68:69], v[66:67], v[64:65]
	v_and_b32_e32 v67, 0xffff0000, v79
	v_and_b32_e32 v66, 0xffff0000, v75
	v_mov_b32_e32 v88, v71
	v_pk_fma_f32 v[64:65], v[88:89], v[66:67], v[64:65]
	s_nop 0
	v_add_f32_e32 v64, v96, v64
	v_add_f32_e32 v64, v64, v65
	v_lshl_add_u32 v65, v80, 2, s95
	ds_write_b32 v65, v64
	v_mbcnt_lo_u32_b32 v64, -1, 0
	v_mbcnt_hi_u32_b32 v64, -1, v64
	s_nop 0
	v_or_b32_e32 v64, s97, v64
	s_nop 0
	v_and_b32_e32 v192, 31, v64
	v_lshrrev_b32_e32 v64, 2, v64
	v_mul_u32_u24_e32 v65, 0x110, v192
	v_and_b32_e32 v64, 8, v64
	v_add3_u32 v196, 0, v65, v64
	v_add_u32_e32 v197, 0x2000, v196
	v_add_u32_e32 v242, 0x4000, v196
	v_add_u32_e32 v243, 0x6000, v196
	ds_read2_b64 v[64:67], v196 offset1:2
	ds_read2_b64 v[206:209], v196 offset0:4 offset1:6
	ds_read2_b64 v[68:71], v197 offset0:64 offset1:66
	ds_read2_b64 v[72:75], v242 offset0:128 offset1:130
	ds_read2_b64 v[76:79], v243 offset0:192 offset1:194
	ds_read2_b64 v[210:213], v197 offset0:68 offset1:70
	ds_read2_b64 v[214:217], v242 offset0:132 offset1:134
	ds_read2_b64 v[218:221], v243 offset0:196 offset1:198
	v_cvt_pk_bf16_f32 v222, v0, v1
	v_cvt_pk_bf16_f32 v223, v2, v3
	v_cvt_pk_bf16_f32 v224, v4, v5
	v_cvt_pk_bf16_f32 v225, v6, v7
	s_waitcnt lgkmcnt(7)
	s_nop 0
	v_mfma_f32_32x32x16_bf16 v[112:127], v[222:225], v[64:67], 0
	s_waitcnt lgkmcnt(5)
	v_mfma_f32_32x32x16_bf16 v[96:111], v[222:225], v[68:71], 0
	s_waitcnt lgkmcnt(4)
	v_mfma_f32_32x32x16_bf16 v[80:95], v[222:225], v[72:75], 0
	s_waitcnt lgkmcnt(3)
	v_mfma_f32_32x32x16_bf16 v[64:79], v[222:225], v[76:79], 0
	ds_read2_b64 v[222:225], v196 offset0:8 offset1:10
	ds_read2_b64 v[226:229], v197 offset0:72 offset1:74
	ds_read2_b64 v[230:233], v242 offset0:136 offset1:138
	ds_read2_b64 v[234:237], v243 offset0:200 offset1:202
	v_cvt_pk_bf16_f32 v238, v8, v9
	v_cvt_pk_bf16_f32 v239, v10, v11
	v_cvt_pk_bf16_f32 v240, v12, v13
	v_cvt_pk_bf16_f32 v241, v14, v15
	s_waitcnt lgkmcnt(6)
	s_nop 0
	v_mfma_f32_32x32x16_bf16 v[96:111], v[238:241], v[210:213], v[96:111]
	s_waitcnt lgkmcnt(5)
	v_mfma_f32_32x32x16_bf16 v[80:95], v[238:241], v[214:217], v[80:95]
	s_waitcnt lgkmcnt(4)
; DI unsigned pk2(float a, float b) { f32x2 f = {a, b}; bf16x2_t h = __builtin_convertvector(f, bf16x2_t); return __builtin_bit_cast(unsigned, h); }
; #define MFMA32(a, b, c) __builtin_amdgcn_mfma_f32_32x32x16_bf16((a), (b), (c), 0, 0, 0)
; template <bool PASS2, int DIRT>
; DI void mlstm_item(const Params& P, LAS unsigned char* lds, int st, int g) {
;     ...
;                 for (int g_ = 0; g_ < 8; ++g_) { const int dkt = g_ >> 1, s2 = g_ & 1;
;                     if (g_ + 1 < 8) ldq(g_ + 1, qf[(g_ + 1) & 1]);
;                     __builtin_amdgcn_sched_barrier(0);
;                     u32x4 xp; xp.x = pk2(C[dkt][8 * s2 + 0], C[dkt][8 * s2 + 1]); xp.y = pk2(C[dkt][8 * s2 + 2], C[dkt][8 * s2 + 3]); xp.z = pk2(C[dkt][8 * s2 + 4], C[dkt][8 * s2 + 5]); xp.w = pk2(C[dkt][8 * s2 + 6], C[dkt][8 * s2 + 7]);
;                     const bf16x8 xs = __builtin_bit_cast(bf16x8, xp);
; #pragma unroll
;                     for (int jt = 0; jt < 4; ++jt) num[jt] = MFMA32(xs, qf[g_ & 1][jt], num[jt]);
;                     __builtin_amdgcn_sched_barrier(0);
;                     if (s2 == 1) asm volatile("" : "+v"(num[0]), "+v"(num[1]), "+v"(num[2]), "+v"(num[3]) :: "memory"); }
;             }
; #pragma unroll
;             for (int jt = 0; jt < 4; ++jt) { const float ws_ = sWST[32 * jt + r];
; #pragma unroll
;                 for (int e = 0; e < 16; ++e) num[jt][e] *= ws_; }
;             __syncthreads();
	v_mfma_f32_32x32x16_bf16 v[64:79], v[238:241], v[218:221], v[64:79]
	v_mfma_f32_32x32x16_bf16 v[112:127], v[238:241], v[206:209], v[112:127]
	ds_read2_b64 v[206:209], v196 offset0:12 offset1:14
	ds_read2_b64 v[210:213], v197 offset0:76 offset1:78
	ds_read2_b64 v[214:217], v242 offset0:140 offset1:142
	ds_read2_b64 v[218:221], v243 offset0:204 offset1:206
	v_cvt_pk_bf16_f32 v238, v16, v17
	v_cvt_pk_bf16_f32 v239, v18, v19
	v_cvt_pk_bf16_f32 v240, v20, v21
	v_cvt_pk_bf16_f32 v241, v22, v23
	s_waitcnt lgkmcnt(6)
	s_nop 0
	v_mfma_f32_32x32x16_bf16 v[96:111], v[238:241], v[226:229], v[96:111]
	s_waitcnt lgkmcnt(5)
	v_mfma_f32_32x32x16_bf16 v[80:95], v[238:241], v[230:233], v[80:95]
	s_waitcnt lgkmcnt(4)
	v_mfma_f32_32x32x16_bf16 v[64:79], v[238:241], v[234:237], v[64:79]
	v_mfma_f32_32x32x16_bf16 v[112:127], v[238:241], v[222:225], v[112:127]
	ds_read2_b64 v[222:225], v196 offset0:16 offset1:18
	ds_read2_b64 v[226:229], v197 offset0:80 offset1:82
	ds_read2_b64 v[230:233], v242 offset0:144 offset1:146
	ds_read2_b64 v[234:237], v243 offset0:208 offset1:210
	v_cvt_pk_bf16_f32 v238, v24, v25
	v_cvt_pk_bf16_f32 v239, v26, v27
	v_cvt_pk_bf16_f32 v240, v28, v29
	v_cvt_pk_bf16_f32 v241, v30, v31
	s_waitcnt lgkmcnt(6)
	s_nop 0
	v_mfma_f32_32x32x16_bf16 v[96:111], v[238:241], v[210:213], v[96:111]
	s_waitcnt lgkmcnt(5)
	v_mfma_f32_32x32x16_bf16 v[80:95], v[238:241], v[214:217], v[80:95]
	s_waitcnt lgkmcnt(4)
	v_mfma_f32_32x32x16_bf16 v[64:79], v[238:241], v[218:221], v[64:79]
	v_mfma_f32_32x32x16_bf16 v[112:127], v[238:241], v[206:209], v[112:127]
	ds_read2_b64 v[206:209], v196 offset0:20 offset1:22
	ds_read2_b64 v[210:213], v197 offset0:84 offset1:86
	ds_read2_b64 v[214:217], v242 offset0:148 offset1:150
	ds_read2_b64 v[218:221], v243 offset0:212 offset1:214
	v_cvt_pk_bf16_f32 v238, v32, v33
	v_cvt_pk_bf16_f32 v239, v34, v35
	v_cvt_pk_bf16_f32 v240, v36, v37
	v_cvt_pk_bf16_f32 v241, v38, v39
	s_waitcnt lgkmcnt(6)
	s_nop 0
	v_mfma_f32_32x32x16_bf16 v[96:111], v[238:241], v[226:229], v[96:111]
	s_waitcnt lgkmcnt(5)
	v_mfma_f32_32x32x16_bf16 v[80:95], v[238:241], v[230:233], v[80:95]
	s_waitcnt lgkmcnt(4)
	v_mfma_f32_32x32x16_bf16 v[64:79], v[238:241], v[234:237], v[64:79]
	v_mfma_f32_32x32x16_bf16 v[112:127], v[238:241], v[222:225], v[112:127]
	ds_read2_b64 v[222:225], v196 offset0:24 offset1:26
	ds_read2_b64 v[226:229], v197 offset0:88 offset1:90
	ds_read2_b64 v[230:233], v242 offset0:152 offset1:154
	ds_read2_b64 v[234:237], v243 offset0:216 offset1:218
	v_cvt_pk_bf16_f32 v238, v40, v41
	v_cvt_pk_bf16_f32 v239, v42, v43
	v_cvt_pk_bf16_f32 v240, v44, v45
	v_cvt_pk_bf16_f32 v241, v46, v47
	s_waitcnt lgkmcnt(6)
	s_nop 0
	v_mfma_f32_32x32x16_bf16 v[96:111], v[238:241], v[210:213], v[96:111]
	s_waitcnt lgkmcnt(5)
	v_mfma_f32_32x32x16_bf16 v[80:95], v[238:241], v[214:217], v[80:95]
	s_waitcnt lgkmcnt(4)
	v_mfma_f32_32x32x16_bf16 v[64:79], v[238:241], v[218:221], v[64:79]
	v_mfma_f32_32x32x16_bf16 v[112:127], v[238:241], v[206:209], v[112:127]
	ds_read2_b64 v[206:209], v196 offset0:28 offset1:30
	ds_read2_b64 v[210:213], v197 offset0:92 offset1:94
	ds_read2_b64 v[214:217], v242 offset0:156 offset1:158
	ds_read2_b64 v[218:221], v243 offset0:220 offset1:222
	v_cvt_pk_bf16_f32 v238, v48, v49
	v_cvt_pk_bf16_f32 v239, v50, v51
	v_cvt_pk_bf16_f32 v240, v52, v53
	v_cvt_pk_bf16_f32 v241, v54, v55
	s_waitcnt lgkmcnt(6)
	s_nop 0
	v_mfma_f32_32x32x16_bf16 v[96:111], v[238:241], v[226:229], v[96:111]
	s_waitcnt lgkmcnt(5)
	v_mfma_f32_32x32x16_bf16 v[80:95], v[238:241], v[230:233], v[80:95]
	s_waitcnt lgkmcnt(4)
	v_mfma_f32_32x32x16_bf16 v[64:79], v[238:241], v[234:237], v[64:79]
	v_mfma_f32_32x32x16_bf16 v[112:127], v[238:241], v[222:225], v[112:127]
	v_cvt_pk_bf16_f32 v222, v56, v57
	v_cvt_pk_bf16_f32 v223, v58, v59
	v_cvt_pk_bf16_f32 v224, v60, v61
	v_cvt_pk_bf16_f32 v225, v62, v63
	s_waitcnt lgkmcnt(2)
	s_nop 0
	v_mfma_f32_32x32x16_bf16 v[96:111], v[222:225], v[210:213], v[96:111]
	s_waitcnt lgkmcnt(1)
	v_mfma_f32_32x32x16_bf16 v[80:95], v[222:225], v[214:217], v[80:95]
	s_waitcnt lgkmcnt(0)
	v_mfma_f32_32x32x16_bf16 v[64:79], v[222:225], v[218:221], v[64:79]
	v_mfma_f32_32x32x16_bf16 v[112:127], v[222:225], v[206:209], v[112:127]
	s_add_i32 s2, 0, 0x19c00
	v_lshl_add_u32 v206, v192, 2, s2
	ds_read2_b32 v[196:197], v206 offset1:32
	s_add_i32 s3, 0, 0x11000
	s_waitcnt lgkmcnt(0)
	s_nop 6
	v_pk_mul_f32 v[126:127], v[196:197], v[126:127] op_sel_hi:[0,1]
	v_pk_mul_f32 v[124:125], v[196:197], v[124:125] op_sel_hi:[0,1]
	v_pk_mul_f32 v[122:123], v[196:197], v[122:123] op_sel_hi:[0,1]
	v_pk_mul_f32 v[120:121], v[196:197], v[120:121] op_sel_hi:[0,1]
	v_pk_mul_f32 v[118:119], v[196:197], v[118:119] op_sel_hi:[0,1]
	v_pk_mul_f32 v[116:117], v[196:197], v[116:117] op_sel_hi:[0,1]
	v_pk_mul_f32 v[114:115], v[196:197], v[114:115] op_sel_hi:[0,1]
	v_pk_mul_f32 v[112:113], v[196:197], v[112:113] op_sel_hi:[0,1]
	v_mov_b32_e32 v192, v197
	ds_read2_b32 v[196:197], v206 offset0:64 offset1:96
	v_pk_mul_f32 v[110:111], v[192:193], v[110:111] op_sel_hi:[0,1]
	v_pk_mul_f32 v[108:109], v[192:193], v[108:109] op_sel_hi:[0,1]
	v_pk_mul_f32 v[106:107], v[192:193], v[106:107] op_sel_hi:[0,1]
	v_pk_mul_f32 v[104:105], v[192:193], v[104:105] op_sel_hi:[0,1]
	v_pk_mul_f32 v[102:103], v[192:193], v[102:103] op_sel_hi:[0,1]
	v_pk_mul_f32 v[100:101], v[192:193], v[100:101] op_sel_hi:[0,1]
	v_pk_mul_f32 v[98:99], v[192:193], v[98:99] op_sel_hi:[0,1]
	v_pk_mul_f32 v[96:97], v[192:193], v[96:97] op_sel_hi:[0,1]
	s_waitcnt lgkmcnt(0)
	v_mov_b32_e32 v192, v197
	v_pk_mul_f32 v[78:79], v[78:79], v[192:193] op_sel_hi:[1,0]
	v_pk_mul_f32 v[76:77], v[76:77], v[192:193] op_sel_hi:[1,0]
	v_pk_mul_f32 v[74:75], v[74:75], v[192:193] op_sel_hi:[1,0]
	v_pk_mul_f32 v[72:73], v[72:73], v[192:193] op_sel_hi:[1,0]
	v_pk_mul_f32 v[70:71], v[70:71], v[192:193] op_sel_hi:[1,0]
	v_pk_mul_f32 v[68:69], v[68:69], v[192:193] op_sel_hi:[1,0]
	v_pk_mul_f32 v[66:67], v[66:67], v[192:193] op_sel_hi:[1,0]
	v_pk_mul_f32 v[64:65], v[64:65], v[192:193] op_sel_hi:[1,0]
	s_barrier
; #define LAS __attribute__((address_space(3)))
; DI int lane_id() { int l; asm volatile("v_mbcnt_lo_u32_b32 %0, -1, 0\n\tv_mbcnt_hi_u32_b32 %0, -1, %0" : "=v"(l)); return l; }
; DI unsigned pk2(float a, float b) { f32x2 f = {a, b}; bf16x2_t h = __builtin_convertvector(f, bf16x2_t); return __builtin_bit_cast(unsigned, h); }
; #define MFMA32(a, b, c) __builtin_amdgcn_mfma_f32_32x32x16_bf16((a), (b), (c), 0, 0, 0)
; template <bool PASS2, int DIRT>
; DI void mlstm_item(const Params& P, LAS unsigned char* lds, int st, int g) {
;     ...
;             tid = (wid << 6) | lane_id(); asm volatile("" : "+v"(tid)); lane = tid & 63; r = lane & 31; hh = lane >> 5;
;             {
;                 bf16x8 pf[2][4];
;                 auto ldp = [&](int ks, bf16x8 (&pb)[4]) {
; #pragma unroll
;                     for (int jt = 0; jt < 4; ++jt) { const bool on = dir ? (ks >= 2 * jt) : (ks <= 2 * jt + 1); if (on) pb[jt] = *(const LAS bf16x8*)(PS + off_b(32 * jt + r, 2 * ks + hh)); } };
;                 ldp(0, pf[0]);
; #pragma unroll
;                 for (int ks = 0; ks < 8; ++ks) {
;                     if (ks + 1 < 8) ldp(ks + 1, pf[(ks + 1) & 1]);
;                     __builtin_amdgcn_sched_barrier(0);
; #pragma unroll
;                     for (int jt = 0; jt < 4; ++jt) { const bool on = dir ? (ks >= 2 * jt) : (ks <= 2 * jt + 1); if (on) num[jt] = MFMA32(vf[ks], pf[ks & 1][jt], num[jt]); }
;                     __builtin_amdgcn_sched_barrier(0); }
;                 asm volatile("" : "+v"(num[0]), "+v"(num[1]), "+v"(num[2]), "+v"(num[3]) :: "memory");
;             }
;             bf16_t* Hd = (bf16_t*)(P.ws + (dir ? WS_HB : WS_HF));
; #pragma unroll
;             for (int jt = 0; jt < 4; ++jt) { const int j = 32 * jt + r;
;                 const float den = (sDENP[j] + sDENP[128 + j]) + (sDENP[256 + j] + sDENP[384 + j]) + sWST[j] * ((sQNP[j] + sQNP[128 + j]) + (sQNP[256 + j] + sQNP[384 + j]));
;                 const float inv = 1.0f / fmaxf(fabsf(den), sCL[j]);
;                 bf16_t* hp = Hd + (size_t)(tok0 + j) * 1024 + h * 256 + 32 * wid + 4 * hh;
; #pragma unroll
;                 for (int gq = 0; gq < 4; ++gq) { u32x2 w; w.x = pk2(num[jt][4 * gq] * inv, num[jt][4 * gq + 1] * inv); w.y = pk2(num[jt][4 * gq + 2] * inv, num[jt][4 * gq + 3] * inv); *(u32x2*)(hp + 8 * gq) = w; } }
	v_mbcnt_lo_u32_b32 v192, -1, 0
	v_mbcnt_hi_u32_b32 v192, -1, v192
	v_pk_mul_f32 v[94:95], v[94:95], v[196:197] op_sel_hi:[1,0]
	v_or_b32_e32 v192, s97, v192
	v_pk_mul_f32 v[92:93], v[92:93], v[196:197] op_sel_hi:[1,0]
	v_and_b32_e32 v206, 31, v192
	v_bfe_u32 v192, v192, 5, 1
	v_pk_mul_f32 v[90:91], v[90:91], v[196:197] op_sel_hi:[1,0]
	v_pk_mul_f32 v[88:89], v[88:89], v[196:197] op_sel_hi:[1,0]
	v_pk_mul_f32 v[86:87], v[86:87], v[196:197] op_sel_hi:[1,0]
	v_pk_mul_f32 v[84:85], v[84:85], v[196:197] op_sel_hi:[1,0]
	v_pk_mul_f32 v[82:83], v[82:83], v[196:197] op_sel_hi:[1,0]
	v_pk_mul_f32 v[80:81], v[80:81], v[196:197] op_sel_hi:[1,0]
	v_mul_u32_u24_e32 v196, 0x110, v206
	v_lshlrev_b32_e32 v197, 4, v192
	v_add3_u32 v196, s3, v197, v196
	ds_read_b128 v[208:211], v196
	ds_read_b128 v[212:215], v196 offset:32
	s_waitcnt vmcnt(7) lgkmcnt(1)
	v_mfma_f32_32x32x16_bf16 v[112:127], v[188:191], v[208:211], v[112:127]
	ds_read_b128 v[208:211], v196 offset:64
	ds_read_b128 v[216:219], v196 offset:8768
	s_waitcnt vmcnt(6) lgkmcnt(2)
	v_mfma_f32_32x32x16_bf16 v[112:127], v[184:187], v[212:215], v[112:127]
	ds_read_b128 v[212:215], v196 offset:96
	ds_read_b128 v[220:223], v196 offset:8800
	s_waitcnt vmcnt(5) lgkmcnt(2)
	v_mfma_f32_32x32x16_bf16 v[96:111], v[180:183], v[216:219], v[96:111]
	v_mfma_f32_32x32x16_bf16 v[112:127], v[180:183], v[208:211], v[112:127]
	ds_read_b128 v[208:211], v196 offset:128
	ds_read_b128 v[216:219], v196 offset:8832
	ds_read_b128 v[224:227], v196 offset:17536
	s_waitcnt vmcnt(4) lgkmcnt(3)
	v_mfma_f32_32x32x16_bf16 v[96:111], v[176:179], v[220:223], v[96:111]
	v_mfma_f32_32x32x16_bf16 v[112:127], v[176:179], v[212:215], v[112:127]
	ds_read_b128 v[212:215], v196 offset:160
	ds_read_b128 v[220:223], v196 offset:8864
	ds_read_b128 v[228:231], v196 offset:17568
	s_waitcnt vmcnt(3) lgkmcnt(4)
	v_mfma_f32_32x32x16_bf16 v[96:111], v[172:175], v[216:219], v[96:111]
	s_waitcnt lgkmcnt(3)
	v_mfma_f32_32x32x16_bf16 v[80:95], v[172:175], v[224:227], v[80:95]
	v_mfma_f32_32x32x16_bf16 v[112:127], v[172:175], v[208:211], v[112:127]
	ds_read_b128 v[208:211], v196 offset:192
	ds_read_b128 v[216:219], v196 offset:8896
	ds_read_b128 v[224:227], v196 offset:17600
	ds_read_b128 v[232:235], v196 offset:26304
	s_waitcnt vmcnt(2) lgkmcnt(5)
	v_mfma_f32_32x32x16_bf16 v[96:111], v[168:171], v[220:223], v[96:111]
	s_waitcnt lgkmcnt(4)
	v_mfma_f32_32x32x16_bf16 v[80:95], v[168:171], v[228:231], v[80:95]
	v_mfma_f32_32x32x16_bf16 v[112:127], v[168:171], v[212:215], v[112:127]
	ds_read_b128 v[212:215], v196 offset:224
	ds_read_b128 v[220:223], v196 offset:8928
	ds_read_b128 v[228:231], v196 offset:17632
	ds_read_b128 v[236:239], v196 offset:26336
	s_waitcnt vmcnt(1) lgkmcnt(6)
	v_mfma_f32_32x32x16_bf16 v[96:111], v[164:167], v[216:219], v[96:111]
	s_waitcnt lgkmcnt(5)
	v_mfma_f32_32x32x16_bf16 v[80:95], v[164:167], v[224:227], v[80:95]
	s_waitcnt lgkmcnt(4)
	v_mfma_f32_32x32x16_bf16 v[64:79], v[164:167], v[232:235], v[64:79]
	v_mfma_f32_32x32x16_bf16 v[112:127], v[164:167], v[208:211], v[112:127]
	s_waitcnt vmcnt(0) lgkmcnt(2)
	v_mfma_f32_32x32x16_bf16 v[96:111], v[160:163], v[220:223], v[96:111]
	s_waitcnt lgkmcnt(1)
	v_mfma_f32_32x32x16_bf16 v[80:95], v[160:163], v[228:231], v[80:95]
	s_waitcnt lgkmcnt(0)
	v_mfma_f32_32x32x16_bf16 v[64:79], v[160:163], v[236:239], v[64:79]
	v_mfma_f32_32x32x16_bf16 v[112:127], v[160:163], v[212:215], v[112:127]
	v_lshlrev_b32_e32 v192, 3, v192
	s_add_i32 s3, 0, 0x1a800
	v_lshlrev_b32_e32 v207, 2, v206
	v_lshl_add_u64 v[196:197], s[14:15], 0, v[192:193]
	v_add_u32_e32 v192, s3, v207
	ds_read_b32 v208, v192
	v_or_b32_e32 v192, 0x200, v207
	v_add_u32_e32 v209, s3, v192
	v_or_b32_e32 v213, 0x400, v207
	v_add_u32_e32 v192, s95, v192
	ds_read_b32 v210, v209
	ds_read_b32 v211, v192
	v_add_u32_e32 v209, s3, v213
	v_or_b32_e32 v215, 0x600, v207
	v_add_u32_e32 v192, s95, v213
	ds_read_b32 v212, v209
	ds_read_b32 v213, v192
	v_add_u32_e32 v209, s3, v215
	v_add_u32_e32 v192, s95, v215
	s_add_i32 s4, 0, 0x19e00
	ds_read_b32 v214, v209
	ds_read_b32 v215, v192
	v_add_u32_e32 v209, s2, v207
	v_add_u32_e32 v192, s4, v207
	ds_read_b32 v216, v209
	ds_read_b32 v192, v192
	v_add_u32_e32 v209, s95, v207
	ds_read_b32 v209, v209
	s_waitcnt lgkmcnt(1)
	v_max_f32_e32 v192, v192, v192
	s_waitcnt lgkmcnt(0)
	v_pk_add_f32 v[208:209], v[208:209], v[210:211]
	v_pk_add_f32 v[210:211], v[212:213], v[214:215]
	s_nop 0
	v_pk_add_f32 v[208:209], v[208:209], v[210:211]
	s_nop 0
	v_fmac_f32_e32 v208, v216, v209
	v_max_f32_e64 v192, |v208|, v192
	v_div_scale_f32 v208, s[44:45], v192, v192, 1.0
	v_rcp_f32_e32 v209, v208
	s_nop 0
	v_fma_f32 v210, -v208, v209, 1.0
	v_fmac_f32_e32 v209, v210, v209
	v_div_scale_f32 v210, vcc, 1.0, v192, 1.0
	v_mul_f32_e32 v211, v210, v209
	v_fma_f32 v212, -v208, v211, v210
	v_fmac_f32_e32 v211, v212, v209
	v_fma_f32 v208, -v208, v211, v210
	v_div_fmas_f32 v208, v208, v209, v211
	v_div_fixup_f32 v208, v208, v192, 1.0
	v_or_b32_e32 v192, s40, v206
	v_lshlrev_b32_e32 v192, 11, v192
	v_pk_mul_f32 v[112:113], v[112:113], v[208:209] op_sel_hi:[1,0]
	v_pk_mul_f32 v[114:115], v[114:115], v[208:209] op_sel_hi:[1,0]
	v_lshl_add_u64 v[210:211], v[196:197], 0, v[192:193]
	v_cvt_pk_bf16_f32 v244, v112, v113
	v_cvt_pk_bf16_f32 v245, v114, v115
	v_pk_mul_f32 v[112:113], v[116:117], v[208:209] op_sel_hi:[1,0]
	v_pk_mul_f32 v[114:115], v[118:119], v[208:209] op_sel_hi:[1,0]
	v_cvt_pk_bf16_f32 v248, v112, v113
	v_cvt_pk_bf16_f32 v249, v114, v115
	v_pk_mul_f32 v[112:113], v[120:121], v[208:209] op_sel_hi:[1,0]
	v_pk_mul_f32 v[114:115], v[122:123], v[208:209] op_sel_hi:[1,0]
	v_cvt_pk_bf16_f32 v246, v112, v113
	v_cvt_pk_bf16_f32 v247, v114, v115
	v_pk_mul_f32 v[112:113], v[124:125], v[208:209] op_sel_hi:[1,0]
	v_pk_mul_f32 v[114:115], v[126:127], v[208:209] op_sel_hi:[1,0]
	v_or_b32_e32 v120, 32, v206
	v_cvt_pk_bf16_f32 v250, v112, v113
	v_cvt_pk_bf16_f32 v251, v114, v115
	v_lshlrev_b32_e32 v121, 2, v120
	v_or_b32_e32 v115, 0x280, v207
	v_mbcnt_lo_u32_b32 v252, -1, 0
	v_mbcnt_hi_u32_b32 v252, -1, v252
	v_lshrrev_b32_e32 v252, 5, v252
	v_mul_u32_u24_e32 v252, 24, v252
	v_mov_b32_e32 v253, 0
	v_permlane32_swap_b32_e32 v244, v246
	v_permlane32_swap_b32_e32 v245, v247
	v_permlane32_swap_b32_e32 v248, v250
	v_permlane32_swap_b32_e32 v249, v251
	v_lshl_add_u64 v[252:253], v[210:211], 0, v[252:253]
	global_store_dwordx4 v[252:253], v[244:247], off
	global_store_dwordx4 v[252:253], v[248:251], off offset:16
	v_add_u32_e32 v112, s3, v121
	v_add_u32_e32 v113, s3, v115
	v_or_b32_e32 v117, 0x480, v207
	v_add_u32_e32 v115, s95, v115
	ds_read_b32 v112, v112
	ds_read_b32 v114, v113
	ds_read_b32 v115, v115
	v_add_u32_e32 v113, s3, v117
	v_or_b32_e32 v119, 0x680, v207
	v_add_u32_e32 v117, s95, v117
	ds_read_b32 v116, v113
	ds_read_b32 v117, v117
	v_add_u32_e32 v113, s3, v119
	v_add_u32_e32 v119, s95, v119
	ds_read_b32 v118, v113
	ds_read_b32 v119, v119
	v_add_u32_e32 v113, s2, v121
	ds_read_b32 v122, v113
	v_add_u32_e32 v113, s95, v121
	ds_read_b32 v113, v113
	s_waitcnt lgkmcnt(0)
; DI unsigned pk2(float a, float b) { f32x2 f = {a, b}; bf16x2_t h = __builtin_convertvector(f, bf16x2_t); return __builtin_bit_cast(unsigned, h); }
; template <bool PASS2, int DIRT>
; DI void mlstm_item(const Params& P, LAS unsigned char* lds, int st, int g) {
;     ...
;             for (int jt = 0; jt < 4; ++jt) { const int j = 32 * jt + r;
;                 const float den = (sDENP[j] + sDENP[128 + j]) + (sDENP[256 + j] + sDENP[384 + j]) + sWST[j] * ((sQNP[j] + sQNP[128 + j]) + (sQNP[256 + j] + sQNP[384 + j]));
;                 const float inv = 1.0f / fmaxf(fabsf(den), sCL[j]);
;                 bf16_t* hp = Hd + (size_t)(tok0 + j) * 1024 + h * 256 + 32 * wid + 4 * hh;
; #pragma unroll
;                 for (int gq = 0; gq < 4; ++gq) { u32x2 w; w.x = pk2(num[jt][4 * gq] * inv, num[jt][4 * gq + 1] * inv); w.y = pk2(num[jt][4 * gq + 2] * inv, num[jt][4 * gq + 3] * inv); *(u32x2*)(hp + 8 * gq) = w; } }
	v_pk_add_f32 v[112:113], v[112:113], v[114:115]
	v_pk_add_f32 v[114:115], v[116:117], v[118:119]
	s_nop 0
	v_pk_add_f32 v[112:113], v[112:113], v[114:115]
	s_nop 0
	v_fmac_f32_e32 v112, v122, v113
	v_add_u32_e32 v113, s4, v121
	ds_read_b32 v113, v113
	s_waitcnt lgkmcnt(0)
	v_max_f32_e32 v113, v113, v113
	v_max_f32_e64 v112, |v112|, v113
	v_div_scale_f32 v113, s[44:45], v112, v112, 1.0
	v_rcp_f32_e32 v114, v113
	s_nop 0
	v_fma_f32 v115, -v113, v114, 1.0
	v_fmac_f32_e32 v114, v115, v114
	v_div_scale_f32 v115, vcc, 1.0, v112, 1.0
	v_mul_f32_e32 v116, v115, v114
	v_fma_f32 v117, -v113, v116, v115
	v_fmac_f32_e32 v116, v117, v114
	v_fma_f32 v113, -v113, v116, v115
	v_div_fmas_f32 v113, v113, v114, v116
	v_div_fixup_f32 v112, v113, v112, 1.0
	v_or_b32_e32 v113, s40, v120
	v_lshlrev_b32_e32 v192, 11, v113
	v_pk_mul_f32 v[96:97], v[96:97], v[112:113] op_sel_hi:[1,0]
	v_pk_mul_f32 v[98:99], v[98:99], v[112:113] op_sel_hi:[1,0]
	v_lshl_add_u64 v[114:115], v[196:197], 0, v[192:193]
	v_cvt_pk_bf16_f32 v244, v96, v97
	v_cvt_pk_bf16_f32 v245, v98, v99
	v_pk_mul_f32 v[96:97], v[100:101], v[112:113] op_sel_hi:[1,0]
	v_pk_mul_f32 v[98:99], v[102:103], v[112:113] op_sel_hi:[1,0]
	v_cvt_pk_bf16_f32 v248, v96, v97
	v_cvt_pk_bf16_f32 v249, v98, v99
	v_pk_mul_f32 v[96:97], v[104:105], v[112:113] op_sel_hi:[1,0]
	v_pk_mul_f32 v[98:99], v[106:107], v[112:113] op_sel_hi:[1,0]
	v_cvt_pk_bf16_f32 v246, v96, v97
	v_cvt_pk_bf16_f32 v247, v98, v99
	v_pk_mul_f32 v[96:97], v[108:109], v[112:113] op_sel_hi:[1,0]
	v_pk_mul_f32 v[98:99], v[110:111], v[112:113] op_sel_hi:[1,0]
	v_or_b32_e32 v104, 64, v206
	v_cvt_pk_bf16_f32 v250, v96, v97
	v_cvt_pk_bf16_f32 v251, v98, v99
	v_lshlrev_b32_e32 v105, 2, v104
	v_or_b32_e32 v99, 0x300, v207
	v_mbcnt_lo_u32_b32 v252, -1, 0
	v_mbcnt_hi_u32_b32 v252, -1, v252
	v_lshrrev_b32_e32 v252, 5, v252
	v_mul_u32_u24_e32 v252, 24, v252
	v_mov_b32_e32 v253, 0
	v_permlane32_swap_b32_e32 v244, v246
	v_permlane32_swap_b32_e32 v245, v247
	v_permlane32_swap_b32_e32 v248, v250
	v_permlane32_swap_b32_e32 v249, v251
	v_lshl_add_u64 v[252:253], v[114:115], 0, v[252:253]
	global_store_dwordx4 v[252:253], v[244:247], off
	global_store_dwordx4 v[252:253], v[248:251], off offset:16
	v_add_u32_e32 v96, s3, v105
	v_add_u32_e32 v97, s3, v99
	v_or_b32_e32 v101, 0x500, v207
	v_add_u32_e32 v99, s95, v99
	ds_read_b32 v96, v96
	ds_read_b32 v98, v97
	ds_read_b32 v99, v99
	v_add_u32_e32 v97, s3, v101
	v_or_b32_e32 v103, 0x700, v207
	v_add_u32_e32 v101, s95, v101
	ds_read_b32 v100, v97
	ds_read_b32 v101, v101
	v_add_u32_e32 v97, s3, v103
	v_add_u32_e32 v103, s95, v103
	ds_read_b32 v102, v97
	ds_read_b32 v103, v103
	v_add_u32_e32 v97, s2, v105
	ds_read_b32 v106, v97
	v_add_u32_e32 v97, s95, v105
	ds_read_b32 v97, v97
	s_waitcnt lgkmcnt(0)
	v_pk_add_f32 v[96:97], v[96:97], v[98:99]
	v_pk_add_f32 v[98:99], v[100:101], v[102:103]
	s_nop 0
	v_pk_add_f32 v[96:97], v[96:97], v[98:99]
	s_nop 0
	v_fmac_f32_e32 v96, v106, v97
	v_add_u32_e32 v97, s4, v105
	ds_read_b32 v97, v97
	s_waitcnt lgkmcnt(0)
	v_max_f32_e32 v97, v97, v97
	v_max_f32_e64 v96, |v96|, v97
	v_div_scale_f32 v97, s[44:45], v96, v96, 1.0
	v_rcp_f32_e32 v98, v97
	s_nop 0
	v_fma_f32 v99, -v97, v98, 1.0
	v_fmac_f32_e32 v98, v99, v98
	v_div_scale_f32 v99, vcc, 1.0, v96, 1.0
	v_mul_f32_e32 v100, v99, v98
	v_fma_f32 v101, -v97, v100, v99
	v_fmac_f32_e32 v100, v101, v98
	v_fma_f32 v97, -v97, v100, v99
	v_div_fmas_f32 v97, v97, v98, v100
	v_div_fixup_f32 v96, v97, v96, 1.0
	v_or_b32_e32 v97, s40, v104
	v_lshlrev_b32_e32 v192, 11, v97
	v_pk_mul_f32 v[80:81], v[80:81], v[96:97] op_sel_hi:[1,0]
	v_pk_mul_f32 v[82:83], v[82:83], v[96:97] op_sel_hi:[1,0]
	v_lshl_add_u64 v[98:99], v[196:197], 0, v[192:193]
	v_cvt_pk_bf16_f32 v244, v80, v81
	v_cvt_pk_bf16_f32 v245, v82, v83
	v_pk_mul_f32 v[80:81], v[84:85], v[96:97] op_sel_hi:[1,0]
	v_pk_mul_f32 v[82:83], v[86:87], v[96:97] op_sel_hi:[1,0]
	v_cvt_pk_bf16_f32 v248, v80, v81
	v_cvt_pk_bf16_f32 v249, v82, v83
	v_pk_mul_f32 v[80:81], v[88:89], v[96:97] op_sel_hi:[1,0]
	v_pk_mul_f32 v[82:83], v[90:91], v[96:97] op_sel_hi:[1,0]
	v_cvt_pk_bf16_f32 v246, v80, v81
	v_cvt_pk_bf16_f32 v247, v82, v83
	v_pk_mul_f32 v[80:81], v[92:93], v[96:97] op_sel_hi:[1,0]
	v_pk_mul_f32 v[82:83], v[94:95], v[96:97] op_sel_hi:[1,0]
	v_or_b32_e32 v88, 0x60, v206
	v_cvt_pk_bf16_f32 v250, v80, v81
	v_cvt_pk_bf16_f32 v251, v82, v83
	v_lshlrev_b32_e32 v89, 2, v88
	v_or_b32_e32 v83, 0x380, v207
	v_mbcnt_lo_u32_b32 v252, -1, 0
	v_mbcnt_hi_u32_b32 v252, -1, v252
	v_lshrrev_b32_e32 v252, 5, v252
	v_mul_u32_u24_e32 v252, 24, v252
	v_mov_b32_e32 v253, 0
	v_permlane32_swap_b32_e32 v244, v246
	v_permlane32_swap_b32_e32 v245, v247
	v_permlane32_swap_b32_e32 v248, v250
	v_permlane32_swap_b32_e32 v249, v251
	v_lshl_add_u64 v[252:253], v[98:99], 0, v[252:253]
	global_store_dwordx4 v[252:253], v[244:247], off
	global_store_dwordx4 v[252:253], v[248:251], off offset:16
	v_add_u32_e32 v80, s3, v89
	v_add_u32_e32 v81, s3, v83
	v_or_b32_e32 v85, 0x580, v207
	v_add_u32_e32 v83, s95, v83
	ds_read_b32 v80, v80
	ds_read_b32 v82, v81
	ds_read_b32 v83, v83
	v_add_u32_e32 v81, s3, v85
	v_or_b32_e32 v87, 0x780, v207
	v_add_u32_e32 v85, s95, v85
	ds_read_b32 v84, v81
	ds_read_b32 v85, v85
	v_add_u32_e32 v81, s3, v87
	v_add_u32_e32 v87, s95, v87
	ds_read_b32 v86, v81
	ds_read_b32 v87, v87
	v_add_u32_e32 v81, s2, v89
	ds_read_b32 v90, v81
	v_add_u32_e32 v81, s95, v89
	ds_read_b32 v81, v81
	s_waitcnt lgkmcnt(0)
; DI int lane_id() { int l; asm volatile("v_mbcnt_lo_u32_b32 %0, -1, 0\n\tv_mbcnt_hi_u32_b32 %0, -1, %0" : "=v"(l)); return l; }
; DI unsigned pk2(float a, float b) { f32x2 f = {a, b}; bf16x2_t h = __builtin_convertvector(f, bf16x2_t); return __builtin_bit_cast(unsigned, h); }
; template <bool PASS2, int DIRT>
; DI void mlstm_item(const Params& P, LAS unsigned char* lds, int st, int g) {
;     ...
;             for (int jt = 0; jt < 4; ++jt) { const int j = 32 * jt + r;
;                 const float den = (sDENP[j] + sDENP[128 + j]) + (sDENP[256 + j] + sDENP[384 + j]) + sWST[j] * ((sQNP[j] + sQNP[128 + j]) + (sQNP[256 + j] + sQNP[384 + j]));
;                 const float inv = 1.0f / fmaxf(fabsf(den), sCL[j]);
;                 bf16_t* hp = Hd + (size_t)(tok0 + j) * 1024 + h * 256 + 32 * wid + 4 * hh;
; #pragma unroll
;                 for (int gq = 0; gq < 4; ++gq) { u32x2 w; w.x = pk2(num[jt][4 * gq] * inv, num[jt][4 * gq + 1] * inv); w.y = pk2(num[jt][4 * gq + 2] * inv, num[jt][4 * gq + 3] * inv); *(u32x2*)(hp + 8 * gq) = w; } }
;         }
;         tid = (wid << 6) | lane_id(); asm volatile("" : "+v"(tid)); lane = tid & 63; r = lane & 31; hh = lane >> 5;
;         if (ci + 1 < nchunks) { const int tokn = chunk_tok0(ci + 1);
; #pragma unroll
;             for (int i = 0; i < 4; ++i) { const int n = tid + 512 * i, row = n >> 4, ch = n & 15; kq[i] = *(const u32x4*)(Kg + (size_t)(tokn + row) * 512 + h * 128 + ch * 8);
;                 if (PASS2) kq[4 + i] = *(const u32x4*)(Qg + (size_t)(tokn + row) * 512 + h * 128 + ch * 8); } }
	v_pk_add_f32 v[80:81], v[80:81], v[82:83]
	v_pk_add_f32 v[82:83], v[84:85], v[86:87]
	s_nop 0
	v_pk_add_f32 v[80:81], v[80:81], v[82:83]
	s_nop 0
	v_fmac_f32_e32 v80, v90, v81
	v_add_u32_e32 v81, s4, v89
	ds_read_b32 v81, v81
	s_add_i32 s4, s72, 1
	s_cmp_lg_u32 s72, 7
	s_waitcnt lgkmcnt(0)
	v_max_f32_e32 v81, v81, v81
	v_max_f32_e64 v80, |v80|, v81
	v_div_scale_f32 v81, s[2:3], v80, v80, 1.0
	v_rcp_f32_e32 v82, v81
	s_mov_b64 s[2:3], -1
	v_fma_f32 v83, -v81, v82, 1.0
	v_fmac_f32_e32 v82, v83, v82
	v_div_scale_f32 v83, vcc, 1.0, v80, 1.0
	v_mul_f32_e32 v84, v83, v82
	v_fma_f32 v85, -v81, v84, v83
	v_fmac_f32_e32 v84, v85, v82
	v_fma_f32 v81, -v81, v84, v83
	v_div_fmas_f32 v81, v81, v82, v84
	v_div_fixup_f32 v80, v81, v80, 1.0
	v_or_b32_e32 v81, s40, v88
	v_lshlrev_b32_e32 v192, 11, v81
	v_pk_mul_f32 v[64:65], v[64:65], v[80:81] op_sel_hi:[1,0]
	v_pk_mul_f32 v[66:67], v[66:67], v[80:81] op_sel_hi:[1,0]
	v_lshl_add_u64 v[82:83], v[196:197], 0, v[192:193]
	v_cvt_pk_bf16_f32 v244, v64, v65
	v_cvt_pk_bf16_f32 v245, v66, v67
	v_pk_mul_f32 v[64:65], v[68:69], v[80:81] op_sel_hi:[1,0]
	v_pk_mul_f32 v[66:67], v[70:71], v[80:81] op_sel_hi:[1,0]
	v_cvt_pk_bf16_f32 v248, v64, v65
	v_cvt_pk_bf16_f32 v249, v66, v67
	v_pk_mul_f32 v[64:65], v[72:73], v[80:81] op_sel_hi:[1,0]
	v_pk_mul_f32 v[66:67], v[74:75], v[80:81] op_sel_hi:[1,0]
	v_cvt_pk_bf16_f32 v246, v64, v65
	v_cvt_pk_bf16_f32 v247, v66, v67
	v_pk_mul_f32 v[64:65], v[76:77], v[80:81] op_sel_hi:[1,0]
	v_pk_mul_f32 v[66:67], v[78:79], v[80:81] op_sel_hi:[1,0]
	v_cvt_pk_bf16_f32 v250, v64, v65
	v_cvt_pk_bf16_f32 v251, v66, v67
	v_mbcnt_lo_u32_b32 v252, -1, 0
	v_mbcnt_hi_u32_b32 v252, -1, v252
	v_lshrrev_b32_e32 v252, 5, v252
	v_mul_u32_u24_e32 v252, 24, v252
	v_mov_b32_e32 v253, 0
	v_permlane32_swap_b32_e32 v244, v246
	v_permlane32_swap_b32_e32 v245, v247
	v_permlane32_swap_b32_e32 v248, v250
	v_permlane32_swap_b32_e32 v249, v251
	v_lshl_add_u64 v[252:253], v[82:83], 0, v[252:253]
	global_store_dwordx4 v[252:253], v[244:247], off
	global_store_dwordx4 v[252:253], v[248:251], off offset:16
	v_mbcnt_lo_u32_b32 v64, -1, 0
	v_mbcnt_hi_u32_b32 v64, -1, v64
	s_nop 0
	v_or_b32_e32 v97, s97, v64
	s_nop 0
	v_lshlrev_b32_e32 v96, 3, v97
	s_cbranch_scc0 .LBB0_759
	s_lshl_b32 s2, s4, 7
	v_lshlrev_b32_e32 v64, 4, v97
	v_add_u32_e32 v72, 0x200, v97
	v_add_u32_e32 v80, 0x400, v97
	v_add_u32_e32 v92, 0x600, v97
	s_sub_i32 s2, s43, s2
	v_and_b32_e32 v192, 0xf0, v64
	v_ashrrev_i32_e32 v64, 4, v97
	v_ashrrev_i32_e32 v72, 4, v72
	v_ashrrev_i32_e32 v80, 4, v80
	v_ashrrev_i32_e32 v92, 4, v92
	v_add_u32_e32 v64, s2, v64
	v_add_u32_e32 v72, s2, v72
	v_add_u32_e32 v80, s2, v80
	v_add_u32_e32 v92, s2, v92
	v_ashrrev_i32_e32 v65, 31, v64
	v_ashrrev_i32_e32 v73, 31, v72
	v_ashrrev_i32_e32 v81, 31, v80
	v_ashrrev_i32_e32 v93, 31, v92
	v_lshl_add_u64 v[88:89], s[6:7], 0, v[192:193]
	v_lshl_add_u64 v[90:91], s[8:9], 0, v[192:193]
	v_lshlrev_b64 v[64:65], 10, v[64:65]
	v_lshlrev_b64 v[72:73], 10, v[72:73]
	v_lshlrev_b64 v[80:81], 10, v[80:81]
	v_lshlrev_b64 v[92:93], 10, v[92:93]
	v_lshl_add_u64 v[66:67], v[88:89], 0, v[64:65]
	v_lshl_add_u64 v[64:65], v[90:91], 0, v[64:65]
	v_lshl_add_u64 v[74:75], v[88:89], 0, v[72:73]
	v_lshl_add_u64 v[72:73], v[90:91], 0, v[72:73]
	v_lshl_add_u64 v[82:83], v[88:89], 0, v[80:81]
	v_lshl_add_u64 v[80:81], v[90:91], 0, v[80:81]
	v_lshl_add_u64 v[88:89], v[88:89], 0, v[92:93]
	v_lshl_add_u64 v[90:91], v[90:91], 0, v[92:93]
	global_load_dwordx4 v[128:131], v[66:67], off
	s_nop 0
	global_load_dwordx4 v[132:135], v[64:65], off
	s_nop 0
	global_load_dwordx4 v[136:139], v[74:75], off
	s_nop 0
	global_load_dwordx4 v[140:143], v[72:73], off
	s_nop 0
	global_load_dwordx4 v[144:147], v[82:83], off
	s_nop 0
	global_load_dwordx4 v[148:151], v[80:81], off
	s_nop 0
	global_load_dwordx4 v[152:155], v[88:89], off
	s_nop 0
	global_load_dwordx4 v[156:159], v[90:91], off
	v_lshlrev_b32_e32 v98, 3, v97
	s_mov_b64 s[2:3], 0

; #define LAS __attribute__((address_space(3)))
; DI unsigned pk2(float a, float b) { f32x2 f = {a, b}; bf16x2_t h = __builtin_convertvector(f, bf16x2_t); return __builtin_bit_cast(unsigned, h); }
; DI float bf_lo(unsigned w) { return __uint_as_float(w << 16); }
; DI float bf_hi(unsigned w) { return __uint_as_float(w & 0xffff0000u); }
; template <bool PASS2, int DIRT>
; DI void mlstm_item(const Params& P, LAS unsigned char* lds, int st, int g) {
;     ...
;         const float a = sMISC[0];
; #pragma unroll
;         for (int dkt = 0; dkt < 4; ++dkt)
; #pragma unroll
;             for (int e = 0; e < 16; ++e) C[dkt][e] *= a;
; #pragma unroll
;         for (int ks = 0; ks < 8; ++ks) { const f32x4 e0 = *(const LAS f32x4*)(sEV + 16 * ks + 8 * hh), e1 = *(const LAS f32x4*)(sEV + 16 * ks + 8 * hh + 4);
;             u32x4 v = __builtin_bit_cast(u32x4, vf[ks]);
;             v.x = pk2(bf_lo(v.x) * e0[0], bf_hi(v.x) * e0[1]); v.y = pk2(bf_lo(v.y) * e0[2], bf_hi(v.y) * e0[3]); v.z = pk2(bf_lo(v.z) * e1[0], bf_hi(v.z) * e1[1]); v.w = pk2(bf_lo(v.w) * e1[2], bf_hi(v.w) * e1[3]);
;             vf[ks] = __builtin_bit_cast(bf16x8, v); }
.LBB0_761:
	v_bfe_u32 v99, v97, 5, 1
	v_mov_b32_e32 v64, s94
	ds_read_b32 v96, v64
	v_lshl_add_u32 v64, v99, 5, 0
	v_add_u32_e32 v102, 0x1a000, v64
	ds_read_b128 v[64:67], v102
	ds_read_b128 v[68:71], v102 offset:16
	v_lshlrev_b32_e32 v72, 16, v188
	v_and_b32_e32 v73, 0xffff0000, v188
	s_waitcnt lgkmcnt(1)
	v_pk_mul_f32 v[64:65], v[64:65], v[72:73]
	v_lshlrev_b32_e32 v72, 16, v189
	v_and_b32_e32 v73, 0xffff0000, v189
	v_pk_mul_f32 v[66:67], v[66:67], v[72:73]
	v_cvt_pk_bf16_f32 v64, v64, v65
	v_cvt_pk_bf16_f32 v65, v66, v67
	v_lshlrev_b32_e32 v66, 16, v190
	v_and_b32_e32 v67, 0xffff0000, v190
	s_waitcnt lgkmcnt(0)
	v_pk_mul_f32 v[66:67], v[68:69], v[66:67]
	v_lshlrev_b32_e32 v68, 16, v191
	v_and_b32_e32 v69, 0xffff0000, v191
	v_pk_mul_f32 v[68:69], v[70:71], v[68:69]
	v_cvt_pk_bf16_f32 v66, v66, v67
	v_cvt_pk_bf16_f32 v67, v68, v69
	ds_read_b128 v[68:71], v102 offset:64
	ds_read_b128 v[72:75], v102 offset:80
	v_lshlrev_b32_e32 v76, 16, v184
	v_and_b32_e32 v77, 0xffff0000, v184
	s_waitcnt lgkmcnt(1)
	v_pk_mul_f32 v[68:69], v[68:69], v[76:77]
	v_lshlrev_b32_e32 v76, 16, v185
	v_and_b32_e32 v77, 0xffff0000, v185
	v_pk_mul_f32 v[70:71], v[70:71], v[76:77]
	v_cvt_pk_bf16_f32 v68, v68, v69
	v_cvt_pk_bf16_f32 v69, v70, v71
	v_lshlrev_b32_e32 v70, 16, v186
	v_and_b32_e32 v71, 0xffff0000, v186
	s_waitcnt lgkmcnt(0)
	v_pk_mul_f32 v[70:71], v[72:73], v[70:71]
	v_lshlrev_b32_e32 v72, 16, v187
	v_and_b32_e32 v73, 0xffff0000, v187
	v_pk_mul_f32 v[72:73], v[74:75], v[72:73]
	v_cvt_pk_bf16_f32 v70, v70, v71
	v_cvt_pk_bf16_f32 v71, v72, v73
	ds_read_b128 v[72:75], v102 offset:128
	ds_read_b128 v[76:79], v102 offset:144
	v_lshlrev_b32_e32 v80, 16, v180
	v_and_b32_e32 v81, 0xffff0000, v180
	s_waitcnt lgkmcnt(1)
	v_pk_mul_f32 v[72:73], v[72:73], v[80:81]
	v_lshlrev_b32_e32 v80, 16, v181
	v_and_b32_e32 v81, 0xffff0000, v181
	v_pk_mul_f32 v[74:75], v[74:75], v[80:81]
	v_cvt_pk_bf16_f32 v72, v72, v73
	v_cvt_pk_bf16_f32 v73, v74, v75
	v_lshlrev_b32_e32 v74, 16, v182
	v_and_b32_e32 v75, 0xffff0000, v182
	s_waitcnt lgkmcnt(0)
	v_pk_mul_f32 v[74:75], v[76:77], v[74:75]
	v_lshlrev_b32_e32 v76, 16, v183
	v_and_b32_e32 v77, 0xffff0000, v183
	v_pk_mul_f32 v[76:77], v[78:79], v[76:77]
	v_cvt_pk_bf16_f32 v74, v74, v75
	v_cvt_pk_bf16_f32 v75, v76, v77
	ds_read_b128 v[76:79], v102 offset:192
	ds_read_b128 v[80:83], v102 offset:208
	v_lshlrev_b32_e32 v84, 16, v176
	v_and_b32_e32 v85, 0xffff0000, v176
	s_waitcnt lgkmcnt(1)
	v_pk_mul_f32 v[76:77], v[76:77], v[84:85]
	v_lshlrev_b32_e32 v84, 16, v177
	v_and_b32_e32 v85, 0xffff0000, v177
	v_pk_mul_f32 v[78:79], v[78:79], v[84:85]
	v_cvt_pk_bf16_f32 v76, v76, v77
	v_cvt_pk_bf16_f32 v77, v78, v79
	v_lshlrev_b32_e32 v78, 16, v178
	v_and_b32_e32 v79, 0xffff0000, v178
	s_waitcnt lgkmcnt(0)
	v_pk_mul_f32 v[78:79], v[80:81], v[78:79]
	v_lshlrev_b32_e32 v80, 16, v179
	v_and_b32_e32 v81, 0xffff0000, v179
	v_pk_mul_f32 v[80:81], v[82:83], v[80:81]
	v_cvt_pk_bf16_f32 v78, v78, v79
	v_cvt_pk_bf16_f32 v79, v80, v81
	ds_read_b128 v[80:83], v102 offset:256
	ds_read_b128 v[84:87], v102 offset:272
	v_lshlrev_b32_e32 v88, 16, v172
	v_and_b32_e32 v89, 0xffff0000, v172
	s_waitcnt lgkmcnt(1)
	v_pk_mul_f32 v[80:81], v[80:81], v[88:89]
	v_lshlrev_b32_e32 v88, 16, v173
	v_and_b32_e32 v89, 0xffff0000, v173
	v_pk_mul_f32 v[82:83], v[82:83], v[88:89]
	v_cvt_pk_bf16_f32 v80, v80, v81
	v_cvt_pk_bf16_f32 v81, v82, v83
	v_lshlrev_b32_e32 v82, 16, v174
	v_and_b32_e32 v83, 0xffff0000, v174
	s_waitcnt lgkmcnt(0)
	v_pk_mul_f32 v[82:83], v[84:85], v[82:83]
	v_lshlrev_b32_e32 v84, 16, v175
	v_and_b32_e32 v85, 0xffff0000, v175
	v_pk_mul_f32 v[84:85], v[86:87], v[84:85]
	v_cvt_pk_bf16_f32 v82, v82, v83
	v_cvt_pk_bf16_f32 v83, v84, v85
	ds_read_b128 v[84:87], v102 offset:320
	ds_read_b128 v[88:91], v102 offset:336
	v_lshlrev_b32_e32 v92, 16, v168
	v_and_b32_e32 v93, 0xffff0000, v168
	s_waitcnt lgkmcnt(1)
	v_pk_mul_f32 v[84:85], v[84:85], v[92:93]
	v_lshlrev_b32_e32 v92, 16, v169
	v_and_b32_e32 v93, 0xffff0000, v169
	v_pk_mul_f32 v[86:87], v[86:87], v[92:93]
	v_cvt_pk_bf16_f32 v84, v84, v85
	v_cvt_pk_bf16_f32 v85, v86, v87
	v_lshlrev_b32_e32 v86, 16, v170
	v_and_b32_e32 v87, 0xffff0000, v170
	s_waitcnt lgkmcnt(0)
	v_pk_mul_f32 v[86:87], v[88:89], v[86:87]
	v_lshlrev_b32_e32 v88, 16, v171
	v_and_b32_e32 v89, 0xffff0000, v171
	v_pk_mul_f32 v[88:89], v[90:91], v[88:89]
	v_cvt_pk_bf16_f32 v86, v86, v87
	v_cvt_pk_bf16_f32 v87, v88, v89
	ds_read_b128 v[88:91], v102 offset:384
	ds_read_b128 v[92:95], v102 offset:400
	v_lshlrev_b32_e32 v100, 16, v164
	v_and_b32_e32 v101, 0xffff0000, v164
	v_lshlrev_b32_e32 v104, 16, v160
	s_waitcnt lgkmcnt(1)
	v_pk_mul_f32 v[88:89], v[88:89], v[100:101]
	v_lshlrev_b32_e32 v100, 16, v165
	v_and_b32_e32 v101, 0xffff0000, v165
	v_pk_mul_f32 v[90:91], v[90:91], v[100:101]
	v_cvt_pk_bf16_f32 v88, v88, v89
	v_cvt_pk_bf16_f32 v89, v90, v91
	v_lshlrev_b32_e32 v90, 16, v166
	v_and_b32_e32 v91, 0xffff0000, v166
	s_waitcnt lgkmcnt(0)
	v_pk_mul_f32 v[90:91], v[92:93], v[90:91]
	v_lshlrev_b32_e32 v92, 16, v167
	v_and_b32_e32 v93, 0xffff0000, v167
	v_pk_mul_f32 v[92:93], v[94:95], v[92:93]
	v_cvt_pk_bf16_f32 v90, v90, v91
	v_cvt_pk_bf16_f32 v91, v92, v93
	ds_read_b128 v[92:95], v102 offset:448
	ds_read_b128 v[100:103], v102 offset:464
	v_and_b32_e32 v105, 0xffff0000, v160
	v_lshlrev_b32_e32 v126, 1, v97
	v_and_b32_e32 v116, 8, v98
	s_waitcnt lgkmcnt(1)
	v_pk_mul_f32 v[92:93], v[92:93], v[104:105]
	v_lshlrev_b32_e32 v104, 16, v161
	v_and_b32_e32 v105, 0xffff0000, v161
	v_pk_mul_f32 v[94:95], v[94:95], v[104:105]
	v_cvt_pk_bf16_f32 v92, v92, v93
	v_cvt_pk_bf16_f32 v93, v94, v95
	v_lshlrev_b32_e32 v94, 16, v162
	v_and_b32_e32 v95, 0xffff0000, v162
	s_waitcnt lgkmcnt(0)
; #define LAS __attribute__((address_space(3)))
; DI unsigned pk2(float a, float b) { f32x2 f = {a, b}; bf16x2_t h = __builtin_convertvector(f, bf16x2_t); return __builtin_bit_cast(unsigned, h); }
; DI float bf_lo(unsigned w) { return __uint_as_float(w << 16); }
; DI float bf_hi(unsigned w) { return __uint_as_float(w & 0xffff0000u); }
; #define MFMA32(a, b, c) __builtin_amdgcn_mfma_f32_32x32x16_bf16((a), (b), (c), 0, 0, 0)
; template <bool PASS2, int DIRT>
; DI void mlstm_item(const Params& P, LAS unsigned char* lds, int st, int g) {
;     ...
; #pragma unroll
;         for (int dkt = 0; dkt < 4; ++dkt)
; #pragma unroll
;             for (int e = 0; e < 16; ++e) C[dkt][e] *= a;
; #pragma unroll
;         for (int ks = 0; ks < 8; ++ks) { const f32x4 e0 = *(const LAS f32x4*)(sEV + 16 * ks + 8 * hh), e1 = *(const LAS f32x4*)(sEV + 16 * ks + 8 * hh + 4);
;             u32x4 v = __builtin_bit_cast(u32x4, vf[ks]);
;             v.x = pk2(bf_lo(v.x) * e0[0], bf_hi(v.x) * e0[1]); v.y = pk2(bf_lo(v.y) * e0[2], bf_hi(v.y) * e0[3]); v.z = pk2(bf_lo(v.z) * e1[0], bf_hi(v.z) * e1[1]); v.w = pk2(bf_lo(v.w) * e1[2], bf_hi(v.w) * e1[3]);
;             vf[ks] = __builtin_bit_cast(bf16x8, v); }
;         { const unsigned blk = (lane >> 4) & 1, q = (lane & 15) >> 2, p = lane & 3;
;           bf16x8 kf[2][4];
;           auto ldk = [&](int ks, bf16x8 (&kb)[4]) {
; #pragma unroll
;               for (int dkt = 0; dkt < 4; ++dkt) {
;                   const s16x4 lo = __builtin_amdgcn_ds_read_tr16_b64_v4i16((LAS s16x4*)(KS + off_b(16 * ks + 8 * hh + q, 4 * dkt + 2 * blk + (p >> 1)) + 8 * (p & 1)));
;                   const s16x4 hi = __builtin_amdgcn_ds_read_tr16_b64_v4i16((LAS s16x4*)(KS + off_b(16 * ks + 8 * hh + 4 + q, 4 * dkt + 2 * blk + (p >> 1)) + 8 * (p & 1)));
;                   kb[dkt] = __builtin_shufflevector(lo, hi, 0, 1, 2, 3, 4, 5, 6, 7); } };
;           ldk(0, kf[0]);
; #pragma unroll
;           for (int ks = 0; ks < 8; ++ks) {
;               if (ks + 1 < 8) ldk(ks + 1, kf[(ks + 1) & 1]);
;               __builtin_amdgcn_sched_barrier(0);
; #pragma unroll
;               for (int dkt = 0; dkt < 4; ++dkt) C[dkt] = MFMA32(kf[ks & 1][dkt], vf[ks], C[dkt]);
;               __builtin_amdgcn_sched_barrier(0); }
;           asm volatile("" : "+v"(C[0]), "+v"(C[1]), "+v"(C[2]), "+v"(C[3]) :: "memory"); }
	v_pk_mul_f32 v[94:95], v[100:101], v[94:95]
	v_lshlrev_b32_e32 v100, 16, v163
	v_and_b32_e32 v101, 0xffff0000, v163
	v_pk_mul_f32 v[100:101], v[102:103], v[100:101]
	v_cvt_pk_bf16_f32 v94, v94, v95
	v_cvt_pk_bf16_f32 v95, v100, v101
	v_bfe_u32 v100, v97, 2, 2
	v_lshl_or_b32 v99, v99, 3, v100
	v_mul_u32_u24_e32 v114, 0x110, v99
	v_and_b32_e32 v99, 32, v126
	v_and_b32_e32 v100, 16, v98
	v_add3_u32 v115, 0, v99, v100
	v_add3_u32 v112, v115, v114, v116
	v_add3_u32 v127, v115, v116, v114
	ds_read_b64_tr_b16 v[98:99], v112 offset:34816
	ds_read_b64_tr_b16 v[100:101], v112 offset:35904
	ds_read_b64_tr_b16 v[102:103], v112 offset:34880
	ds_read_b64_tr_b16 v[104:105], v112 offset:35968
	ds_read_b64_tr_b16 v[106:107], v112 offset:34944
	ds_read_b64_tr_b16 v[108:109], v112 offset:36032
	ds_read_b64_tr_b16 v[110:111], v112 offset:35008
	ds_read_b64_tr_b16 v[112:113], v112 offset:36096
	ds_read_b64_tr_b16 v[114:115], v127 offset:39168
	ds_read_b64_tr_b16 v[116:117], v127 offset:40256
	ds_read_b64_tr_b16 v[118:119], v127 offset:39232
	ds_read_b64_tr_b16 v[120:121], v127 offset:40320
	ds_read_b64_tr_b16 v[122:123], v127 offset:39296
	ds_read_b64_tr_b16 v[124:125], v127 offset:40384
	ds_read_b64_tr_b16 v[160:161], v127 offset:39360
	ds_read_b64_tr_b16 v[162:163], v127 offset:40448
	v_pk_mul_f32 v[14:15], v[14:15], v[96:97] op_sel_hi:[1,0]
	v_pk_mul_f32 v[12:13], v[12:13], v[96:97] op_sel_hi:[1,0]
	v_pk_mul_f32 v[10:11], v[10:11], v[96:97] op_sel_hi:[1,0]
	v_pk_mul_f32 v[8:9], v[8:9], v[96:97] op_sel_hi:[1,0]
	v_pk_mul_f32 v[6:7], v[6:7], v[96:97] op_sel_hi:[1,0]
	v_pk_mul_f32 v[4:5], v[4:5], v[96:97] op_sel_hi:[1,0]
	v_pk_mul_f32 v[2:3], v[2:3], v[96:97] op_sel_hi:[1,0]
	v_pk_mul_f32 v[0:1], v[0:1], v[96:97] op_sel_hi:[1,0]
	v_pk_mul_f32 v[30:31], v[30:31], v[96:97] op_sel_hi:[1,0]
	v_pk_mul_f32 v[28:29], v[28:29], v[96:97] op_sel_hi:[1,0]
	v_pk_mul_f32 v[26:27], v[26:27], v[96:97] op_sel_hi:[1,0]
	v_pk_mul_f32 v[24:25], v[24:25], v[96:97] op_sel_hi:[1,0]
	v_pk_mul_f32 v[22:23], v[22:23], v[96:97] op_sel_hi:[1,0]
	v_pk_mul_f32 v[20:21], v[20:21], v[96:97] op_sel_hi:[1,0]
	v_pk_mul_f32 v[18:19], v[18:19], v[96:97] op_sel_hi:[1,0]
	v_pk_mul_f32 v[16:17], v[16:17], v[96:97] op_sel_hi:[1,0]
	v_pk_mul_f32 v[46:47], v[46:47], v[96:97] op_sel_hi:[1,0]
	v_pk_mul_f32 v[44:45], v[44:45], v[96:97] op_sel_hi:[1,0]
	v_pk_mul_f32 v[42:43], v[42:43], v[96:97] op_sel_hi:[1,0]
	v_pk_mul_f32 v[40:41], v[40:41], v[96:97] op_sel_hi:[1,0]
	v_pk_mul_f32 v[38:39], v[38:39], v[96:97] op_sel_hi:[1,0]
	v_pk_mul_f32 v[36:37], v[36:37], v[96:97] op_sel_hi:[1,0]
	v_pk_mul_f32 v[34:35], v[34:35], v[96:97] op_sel_hi:[1,0]
	v_pk_mul_f32 v[32:33], v[32:33], v[96:97] op_sel_hi:[1,0]
	v_pk_mul_f32 v[62:63], v[62:63], v[96:97] op_sel_hi:[1,0]
	v_pk_mul_f32 v[60:61], v[60:61], v[96:97] op_sel_hi:[1,0]
	v_pk_mul_f32 v[58:59], v[58:59], v[96:97] op_sel_hi:[1,0]
	v_pk_mul_f32 v[56:57], v[56:57], v[96:97] op_sel_hi:[1,0]
	v_pk_mul_f32 v[54:55], v[54:55], v[96:97] op_sel_hi:[1,0]
	v_pk_mul_f32 v[52:53], v[52:53], v[96:97] op_sel_hi:[1,0]
	v_pk_mul_f32 v[50:51], v[50:51], v[96:97] op_sel_hi:[1,0]
	v_pk_mul_f32 v[48:49], v[48:49], v[96:97] op_sel_hi:[1,0]
	s_mov_b32 s2, 32
	v_add_u32_e32 v164, 0x7b40, v127
	s_waitcnt lgkmcnt(14)
	v_mfma_f32_32x32x16_bf16 v[0:15], v[98:101], v[64:67], v[0:15]
	s_waitcnt lgkmcnt(12)
	v_mfma_f32_32x32x16_bf16 v[16:31], v[102:105], v[64:67], v[16:31]
	s_waitcnt lgkmcnt(10)
	v_mfma_f32_32x32x16_bf16 v[32:47], v[106:109], v[64:67], v[32:47]
	s_waitcnt lgkmcnt(8)
	v_mfma_f32_32x32x16_bf16 v[48:63], v[110:113], v[64:67], v[48:63]
	ds_read_b64_tr_b16 v[64:65], v127 offset:43520
	ds_read_b64_tr_b16 v[98:99], v127 offset:43584
	ds_read_b64_tr_b16 v[102:103], v127 offset:43648
	ds_read_b64_tr_b16 v[106:107], v127 offset:43712
	ds_read_b64_tr_b16 v[66:67], v127 offset:44608
	ds_read_b64_tr_b16 v[100:101], v127 offset:44672
	ds_read_b64_tr_b16 v[104:105], v127 offset:44736
	ds_read_b64_tr_b16 v[108:109], v127 offset:44800
	s_waitcnt lgkmcnt(14)
	v_mfma_f32_32x32x16_bf16 v[0:15], v[114:117], v[68:71], v[0:15]
	s_waitcnt lgkmcnt(12)
	v_mfma_f32_32x32x16_bf16 v[16:31], v[118:121], v[68:71], v[16:31]
	s_waitcnt lgkmcnt(10)
	v_mfma_f32_32x32x16_bf16 v[32:47], v[122:125], v[68:71], v[32:47]
	s_waitcnt lgkmcnt(8)
; #define LAS __attribute__((address_space(3)))
; DI float bf2f(unsigned short s) { return __uint_as_float(((unsigned)s) << 16); }
; #define MFMA32(a, b, c) __builtin_amdgcn_mfma_f32_32x32x16_bf16((a), (b), (c), 0, 0, 0)
; template <bool PASS2, int DIRT>
; DI void mlstm_item(const Params& P, LAS unsigned char* lds, int st, int g) {
;     ...
;           ldk(0, kf[0]);
; #pragma unroll
;           for (int ks = 0; ks < 8; ++ks) {
;               if (ks + 1 < 8) ldk(ks + 1, kf[(ks + 1) & 1]);
;               __builtin_amdgcn_sched_barrier(0);
; #pragma unroll
;               for (int dkt = 0; dkt < 4; ++dkt) C[dkt] = MFMA32(kf[ks & 1][dkt], vf[ks], C[dkt]);
;               __builtin_amdgcn_sched_barrier(0); }
;           asm volatile("" : "+v"(C[0]), "+v"(C[1]), "+v"(C[2]), "+v"(C[3]) :: "memory"); }
;         { const int dk = tid & 127, part = tid >> 7; float s = 0.f;
; #pragma unroll 8
;           for (int i = 0; i < 32; ++i) { const int sp = 32 * part + i; s += sEV[sp] * bf2f(*(const LAS unsigned short*)(KS + off_b(sp, dk >> 3) + (dk & 7) * 2)); }
;           sNPART[part * 128 + dk] = s; }
	v_mfma_f32_32x32x16_bf16 v[48:63], v[160:163], v[68:71], v[48:63]
	ds_read_b64_tr_b16 v[68:69], v127 offset:47872
	ds_read_b64_tr_b16 v[110:111], v127 offset:47936
	ds_read_b64_tr_b16 v[114:115], v127 offset:48000
	ds_read_b64_tr_b16 v[118:119], v127 offset:48064
	ds_read_b64_tr_b16 v[70:71], v127 offset:48960
	ds_read_b64_tr_b16 v[112:113], v127 offset:49024
	ds_read_b64_tr_b16 v[116:117], v127 offset:49088
	ds_read_b64_tr_b16 v[120:121], v127 offset:49152
	s_waitcnt lgkmcnt(11)
	v_mfma_f32_32x32x16_bf16 v[0:15], v[64:67], v[72:75], v[0:15]
	s_waitcnt lgkmcnt(10)
	v_mfma_f32_32x32x16_bf16 v[16:31], v[98:101], v[72:75], v[16:31]
	s_waitcnt lgkmcnt(9)
	v_mfma_f32_32x32x16_bf16 v[32:47], v[102:105], v[72:75], v[32:47]
	s_waitcnt lgkmcnt(8)
	v_mfma_f32_32x32x16_bf16 v[48:63], v[106:109], v[72:75], v[48:63]
	ds_read_b64_tr_b16 v[64:65], v127 offset:52224
	ds_read_b64_tr_b16 v[72:73], v127 offset:52288
	ds_read_b64_tr_b16 v[98:99], v127 offset:52352
	ds_read_b64_tr_b16 v[102:103], v127 offset:52416
	ds_read_b64_tr_b16 v[66:67], v127 offset:53312
	ds_read_b64_tr_b16 v[74:75], v127 offset:53376
	ds_read_b64_tr_b16 v[100:101], v127 offset:53440
	ds_read_b64_tr_b16 v[104:105], v127 offset:53504
	s_waitcnt lgkmcnt(11)
	v_mfma_f32_32x32x16_bf16 v[0:15], v[68:71], v[76:79], v[0:15]
	s_waitcnt lgkmcnt(10)
	v_mfma_f32_32x32x16_bf16 v[16:31], v[110:113], v[76:79], v[16:31]
	s_waitcnt lgkmcnt(9)
	v_mfma_f32_32x32x16_bf16 v[32:47], v[114:117], v[76:79], v[32:47]
	s_waitcnt lgkmcnt(8)
	v_mfma_f32_32x32x16_bf16 v[48:63], v[118:121], v[76:79], v[48:63]
	ds_read_b64_tr_b16 v[68:69], v127 offset:56576
	ds_read_b64_tr_b16 v[76:77], v127 offset:56640
	ds_read_b64_tr_b16 v[106:107], v127 offset:56704
	ds_read_b64_tr_b16 v[110:111], v127 offset:56768
	ds_read_b64_tr_b16 v[70:71], v127 offset:57664
	ds_read_b64_tr_b16 v[78:79], v127 offset:57728
	ds_read_b64_tr_b16 v[108:109], v127 offset:57792
	ds_read_b64_tr_b16 v[112:113], v127 offset:57856
	s_waitcnt lgkmcnt(11)
	v_mfma_f32_32x32x16_bf16 v[0:15], v[64:67], v[80:83], v[0:15]
	s_waitcnt lgkmcnt(10)
	v_mfma_f32_32x32x16_bf16 v[16:31], v[72:75], v[80:83], v[16:31]
	s_waitcnt lgkmcnt(9)
	v_mfma_f32_32x32x16_bf16 v[32:47], v[98:101], v[80:83], v[32:47]
	s_waitcnt lgkmcnt(8)
	v_mfma_f32_32x32x16_bf16 v[48:63], v[102:105], v[80:83], v[48:63]
	ds_read_b64_tr_b16 v[64:65], v127 offset:60928
	ds_read_b64_tr_b16 v[72:73], v127 offset:60992
	ds_read_b64_tr_b16 v[80:81], v127 offset:61056
	ds_read_b64_tr_b16 v[98:99], v127 offset:61120
	ds_read_b64_tr_b16 v[66:67], v127 offset:62016
	ds_read_b64_tr_b16 v[74:75], v127 offset:62080
	ds_read_b64_tr_b16 v[82:83], v127 offset:62144
	ds_read_b64_tr_b16 v[100:101], v127 offset:62208
	s_waitcnt lgkmcnt(11)
	v_mfma_f32_32x32x16_bf16 v[0:15], v[68:71], v[84:87], v[0:15]
	s_waitcnt lgkmcnt(10)
	v_mfma_f32_32x32x16_bf16 v[16:31], v[76:79], v[84:87], v[16:31]
	s_waitcnt lgkmcnt(9)
	v_mfma_f32_32x32x16_bf16 v[32:47], v[106:109], v[84:87], v[32:47]
	s_waitcnt lgkmcnt(8)
	v_mfma_f32_32x32x16_bf16 v[48:63], v[110:113], v[84:87], v[48:63]
	ds_read_b64_tr_b16 v[68:69], v127 offset:65280
	ds_read_b64_tr_b16 v[76:77], v127 offset:65344
	ds_read_b64_tr_b16 v[84:85], v127 offset:65408
	ds_read_b64_tr_b16 v[102:103], v127 offset:65472
	ds_read_b64_tr_b16 v[70:71], v164 offset:34816
	ds_read_b64_tr_b16 v[78:79], v164 offset:34880
	ds_read_b64_tr_b16 v[86:87], v164 offset:34944
	ds_read_b64_tr_b16 v[104:105], v164 offset:35008
	s_waitcnt lgkmcnt(11)
	v_mfma_f32_32x32x16_bf16 v[0:15], v[64:67], v[88:91], v[0:15]
	s_waitcnt lgkmcnt(10)
	v_mfma_f32_32x32x16_bf16 v[16:31], v[72:75], v[88:91], v[16:31]
	s_waitcnt lgkmcnt(9)
	v_mfma_f32_32x32x16_bf16 v[32:47], v[80:83], v[88:91], v[32:47]
	s_waitcnt lgkmcnt(8)
	v_mfma_f32_32x32x16_bf16 v[48:63], v[98:101], v[88:91], v[48:63]
	s_waitcnt lgkmcnt(3)
	v_mfma_f32_32x32x16_bf16 v[0:15], v[68:71], v[92:95], v[0:15]
	s_waitcnt lgkmcnt(2)
	v_mfma_f32_32x32x16_bf16 v[16:31], v[76:79], v[92:95], v[16:31]
	s_waitcnt lgkmcnt(1)
	v_mfma_f32_32x32x16_bf16 v[32:47], v[84:87], v[92:95], v[32:47]
	s_waitcnt lgkmcnt(0)
	v_mfma_f32_32x32x16_bf16 v[48:63], v[102:105], v[92:95], v[48:63]
	v_ashrrev_i32_e32 v64, 2, v97
	v_lshrrev_b32_e32 v64, 5, v64
	v_and_b32_e32 v65, 0xf0, v126
	v_and_b32_e32 v66, 14, v126
	v_mul_lo_u32 v67, v64, s64
	v_or3_b32 v65, v67, v65, v66
	v_add_u32_e32 v65, 0x8800, v65
	v_lshlrev_b32_e32 v66, 7, v64
	v_mov_b32_e32 v64, 0

; #define LAS __attribute__((address_space(3)))
; template <bool PASS2, int DIRT>
; DI void mlstm_item(const Params& P, LAS unsigned char* lds, int st, int g) {
;     ...
;             { const int j = tid & 127, part = tid >> 7; float s = 0.f;
; #pragma unroll
;               for (int cc = 0; cc < 4; ++cc) { const u32x4 q8 = *(const LAS u32x4*)(QS + off_b(j, 4 * part + cc)); const f32x4 n0a = *(const LAS f32x4*)(sN0 + 32 * part + 8 * cc), n0b = *(const LAS f32x4*)(sN0 + 32 * part + 8 * cc + 4);
;                   s += bf_lo(q8.x) * n0a[0] + bf_hi(q8.x) * n0a[1] + bf_lo(q8.y) * n0a[2] + bf_hi(q8.y) * n0a[3] + bf_lo(q8.z) * n0b[0] + bf_hi(q8.z) * n0b[1] + bf_lo(q8.w) * n0b[2] + bf_hi(q8.w) * n0b[3]; }
;               sQNP[part * 128 + j] = s; }
;             tid = (wid << 6) | lane_id(); asm volatile("" : "+v"(tid)); lane = tid & 63; r = lane & 31; hh = lane >> 5;
; #pragma unroll
;             for (int jt = 0; jt < 4; ++jt)
; #pragma unroll
;                 for (int e = 0; e < 16; ++e) num[jt][e] = 0.f;
;             {
;                 bf16x8 qf[2][4];
;                 auto ldq = [&](int g_, bf16x8 (&qb)[4]) { const int dkt = g_ >> 1, s2 = g_ & 1;
; #pragma unroll
;                     for (int jt = 0; jt < 4; ++jt) { const s16x4 lo = *(const LAS s16x4*)(QS + off_b(32 * jt + r, 4 * dkt + 2 * s2) + 8 * hh); const s16x4 hi = *(const LAS s16x4*)(QS + off_b(32 * jt + r, 4 * dkt + 2 * s2 + 1) + 8 * hh);
;                         qb[jt] = __builtin_shufflevector(lo, hi, 0, 1, 2, 3, 4, 5, 6, 7); } };
;                 ldq(0, qf[0]);
; #pragma unroll
;                 for (int g_ = 0; g_ < 8; ++g_) { const int dkt = g_ >> 1, s2 = g_ & 1;
;                     if (g_ + 1 < 8) ldq(g_ + 1, qf[(g_ + 1) & 1]);
;                     __builtin_amdgcn_sched_barrier(0);
;                     u32x4 xp; xp.x = pk2(C[dkt][8 * s2 + 0], C[dkt][8 * s2 + 1]); xp.y = pk2(C[dkt][8 * s2 + 2], C[dkt][8 * s2 + 3]); xp.z = pk2(C[dkt][8 * s2 + 4], C[dkt][8 * s2 + 5]); xp.w = pk2(C[dkt][8 * s2 + 6], C[dkt][8 * s2 + 7]);
;                     const bf16x8 xs = __builtin_bit_cast(bf16x8, xp);
; #pragma unroll
;                     for (int jt = 0; jt < 4; ++jt) num[jt] = MFMA32(xs, qf[g_ & 1][jt], num[jt]);
;                     __builtin_amdgcn_sched_barrier(0);
;                     if (s2 == 1) asm volatile("" : "+v"(num[0]), "+v"(num[1]), "+v"(num[2]), "+v"(num[3]) :: "memory"); }
.LBB0_808:
	s_and_saveexec_b64 s[4:5], s[2:3]
	v_lshl_add_u32 v65, v90, 2, s1
	ds_write_b32 v65, v64
	s_or_b64 exec, exec, s[4:5]
	v_and_b32_e32 v65, 0xffffff80, v80
	v_add_u32_e32 v65, 0, v65
	v_and_b32_e32 v64, 0x7f, v80
	v_add_u32_e32 v81, 0x1a600, v65
	v_ashrrev_i32_e32 v65, 1, v80
	v_mul_u32_u24_e32 v64, 0x110, v64
	v_and_b32_e32 v65, 0xffffffc0, v65
	v_add3_u32 v76, 0, v64, v65
	s_waitcnt lgkmcnt(1)
	ds_read_b128 v[64:67], v76
	ds_read_b128 v[68:71], v76 offset:16
	ds_read_b128 v[72:75], v76 offset:32
	ds_read_b128 v[76:79], v76 offset:48
	ds_read_b128 v[82:85], v81
	ds_read_b128 v[86:89], v81 offset:16
	ds_read_b128 v[90:93], v81 offset:32
	ds_read_b128 v[94:97], v81 offset:48
	s_waitcnt lgkmcnt(6)
	v_and_b32_e32 v103, 0xffff0000, v68
	v_and_b32_e32 v102, 0xffff0000, v64
	v_lshlrev_b32_e32 v99, 16, v68
	s_waitcnt lgkmcnt(1)
	v_mov_b32_e32 v101, v90
	v_mov_b32_e32 v90, v83
	v_lshlrev_b32_e32 v98, 16, v64
	v_mov_b32_e32 v100, v82
	v_pk_mul_f32 v[82:83], v[90:91], v[102:103]
	v_lshlrev_b32_e32 v91, 16, v69
	v_pk_fma_f32 v[82:83], v[100:101], v[98:99], v[82:83]
	v_lshlrev_b32_e32 v90, 16, v65
	v_mov_b32_e32 v98, v84
	v_mov_b32_e32 v99, v92
	v_pk_fma_f32 v[82:83], v[98:99], v[90:91], v[82:83]
	v_and_b32_e32 v69, 0xffff0000, v69
	v_and_b32_e32 v68, 0xffff0000, v65
	v_mov_b32_e32 v92, v85
	v_pk_fma_f32 v[64:65], v[92:93], v[68:69], v[82:83]
	v_lshlrev_b32_e32 v69, 16, v70
	v_lshlrev_b32_e32 v68, 16, v66
	v_mov_b32_e32 v82, v86
	s_waitcnt lgkmcnt(0)
	v_mov_b32_e32 v83, v94
	v_pk_fma_f32 v[64:65], v[82:83], v[68:69], v[64:65]
	v_and_b32_e32 v69, 0xffff0000, v70
	v_and_b32_e32 v68, 0xffff0000, v66
	v_mov_b32_e32 v94, v87
	v_pk_fma_f32 v[64:65], v[94:95], v[68:69], v[64:65]
	v_lshlrev_b32_e32 v69, 16, v71
	v_lshlrev_b32_e32 v68, 16, v67
	v_mov_b32_e32 v82, v88
	v_mov_b32_e32 v83, v96
	v_pk_fma_f32 v[64:65], v[82:83], v[68:69], v[64:65]
	v_and_b32_e32 v69, 0xffff0000, v71
	v_and_b32_e32 v68, 0xffff0000, v67
	v_mov_b32_e32 v96, v89
	v_pk_fma_f32 v[64:65], v[96:97], v[68:69], v[64:65]
	v_and_b32_e32 v95, 0xffff0000, v76
	v_add_f32_e32 v64, 0, v64
	v_add_f32_e32 v96, v64, v65
	ds_read_b128 v[64:67], v81 offset:64
	ds_read_b128 v[68:71], v81 offset:80
	ds_read_b128 v[82:85], v81 offset:96
	ds_read_b128 v[86:89], v81 offset:112
	v_and_b32_e32 v94, 0xffff0000, v72
	v_lshlrev_b32_e32 v91, 16, v76
	v_lshlrev_b32_e32 v90, 16, v72
	s_waitcnt lgkmcnt(1)
	v_mov_b32_e32 v93, v82
	v_mov_b32_e32 v82, v65
	v_mov_b32_e32 v92, v64
	v_pk_mul_f32 v[64:65], v[82:83], v[94:95]
	v_lshlrev_b32_e32 v83, 16, v77
	v_pk_fma_f32 v[64:65], v[92:93], v[90:91], v[64:65]
	v_lshlrev_b32_e32 v82, 16, v73
	v_mov_b32_e32 v90, v66
	v_mov_b32_e32 v91, v84
	v_pk_fma_f32 v[64:65], v[90:91], v[82:83], v[64:65]
	v_and_b32_e32 v77, 0xffff0000, v77
	v_and_b32_e32 v76, 0xffff0000, v73
	v_mov_b32_e32 v84, v67
	v_pk_fma_f32 v[64:65], v[84:85], v[76:77], v[64:65]
	v_lshlrev_b32_e32 v67, 16, v78
	v_lshlrev_b32_e32 v66, 16, v74
	v_mov_b32_e32 v72, v68
	s_waitcnt lgkmcnt(0)
	v_mov_b32_e32 v73, v86
	v_pk_fma_f32 v[64:65], v[72:73], v[66:67], v[64:65]
	v_and_b32_e32 v67, 0xffff0000, v78
	v_and_b32_e32 v66, 0xffff0000, v74
	v_mov_b32_e32 v86, v69
	v_pk_fma_f32 v[64:65], v[86:87], v[66:67], v[64:65]
	v_lshlrev_b32_e32 v67, 16, v79
	v_lshlrev_b32_e32 v66, 16, v75
	v_mov_b32_e32 v68, v70
	v_mov_b32_e32 v69, v88
	v_pk_fma_f32 v[64:65], v[68:69], v[66:67], v[64:65]
	v_and_b32_e32 v67, 0xffff0000, v79
	v_and_b32_e32 v66, 0xffff0000, v75
	v_mov_b32_e32 v88, v71
	v_pk_fma_f32 v[64:65], v[88:89], v[66:67], v[64:65]
	s_nop 0
	v_add_f32_e32 v64, v96, v64
	v_add_f32_e32 v64, v64, v65
	v_lshl_add_u32 v65, v80, 2, s95
	ds_write_b32 v65, v64
	v_mbcnt_lo_u32_b32 v64, -1, 0
	v_mbcnt_hi_u32_b32 v64, -1, v64
	s_nop 0
	v_or_b32_e32 v64, s97, v64
	s_nop 0
	v_and_b32_e32 v192, 31, v64
	v_lshrrev_b32_e32 v64, 2, v64
	v_mul_u32_u24_e32 v65, 0x110, v192
	v_and_b32_e32 v64, 8, v64
	v_add3_u32 v195, 0, v65, v64
	v_add_u32_e32 v196, 0x2000, v195
	v_add_u32_e32 v197, 0x4000, v195
	v_add_u32_e32 v242, 0x6000, v195
	ds_read2_b64 v[64:67], v195 offset1:2
	ds_read2_b64 v[206:209], v195 offset0:4 offset1:6
	ds_read2_b64 v[68:71], v196 offset0:64 offset1:66
	ds_read2_b64 v[72:75], v197 offset0:128 offset1:130
	ds_read2_b64 v[76:79], v242 offset0:192 offset1:194
	ds_read2_b64 v[210:213], v196 offset0:68 offset1:70
	ds_read2_b64 v[214:217], v197 offset0:132 offset1:134
	ds_read2_b64 v[218:221], v242 offset0:196 offset1:198
	v_cvt_pk_bf16_f32 v222, v0, v1
	v_cvt_pk_bf16_f32 v223, v2, v3
	v_cvt_pk_bf16_f32 v224, v4, v5
	v_cvt_pk_bf16_f32 v225, v6, v7
	s_waitcnt lgkmcnt(7)
	s_nop 0
	v_mfma_f32_32x32x16_bf16 v[112:127], v[222:225], v[64:67], 0
	s_waitcnt lgkmcnt(5)
	v_mfma_f32_32x32x16_bf16 v[96:111], v[222:225], v[68:71], 0
	s_waitcnt lgkmcnt(4)
	v_mfma_f32_32x32x16_bf16 v[80:95], v[222:225], v[72:75], 0
	s_waitcnt lgkmcnt(3)
	v_mfma_f32_32x32x16_bf16 v[64:79], v[222:225], v[76:79], 0
	ds_read2_b64 v[222:225], v195 offset0:8 offset1:10
	ds_read2_b64 v[226:229], v196 offset0:72 offset1:74
	ds_read2_b64 v[230:233], v197 offset0:136 offset1:138
	ds_read2_b64 v[234:237], v242 offset0:200 offset1:202
	v_cvt_pk_bf16_f32 v238, v8, v9
	v_cvt_pk_bf16_f32 v239, v10, v11
	v_cvt_pk_bf16_f32 v240, v12, v13
	v_cvt_pk_bf16_f32 v241, v14, v15
	s_waitcnt lgkmcnt(6)
	s_nop 0
	v_mfma_f32_32x32x16_bf16 v[96:111], v[238:241], v[210:213], v[96:111]
	s_waitcnt lgkmcnt(5)
	v_mfma_f32_32x32x16_bf16 v[80:95], v[238:241], v[214:217], v[80:95]
	s_waitcnt lgkmcnt(4)
; DI unsigned pk2(float a, float b) { f32x2 f = {a, b}; bf16x2_t h = __builtin_convertvector(f, bf16x2_t); return __builtin_bit_cast(unsigned, h); }
; #define MFMA32(a, b, c) __builtin_amdgcn_mfma_f32_32x32x16_bf16((a), (b), (c), 0, 0, 0)
; template <bool PASS2, int DIRT>
; DI void mlstm_item(const Params& P, LAS unsigned char* lds, int st, int g) {
;     ...
;                 for (int g_ = 0; g_ < 8; ++g_) { const int dkt = g_ >> 1, s2 = g_ & 1;
;                     if (g_ + 1 < 8) ldq(g_ + 1, qf[(g_ + 1) & 1]);
;                     __builtin_amdgcn_sched_barrier(0);
;                     u32x4 xp; xp.x = pk2(C[dkt][8 * s2 + 0], C[dkt][8 * s2 + 1]); xp.y = pk2(C[dkt][8 * s2 + 2], C[dkt][8 * s2 + 3]); xp.z = pk2(C[dkt][8 * s2 + 4], C[dkt][8 * s2 + 5]); xp.w = pk2(C[dkt][8 * s2 + 6], C[dkt][8 * s2 + 7]);
;                     const bf16x8 xs = __builtin_bit_cast(bf16x8, xp);
; #pragma unroll
;                     for (int jt = 0; jt < 4; ++jt) num[jt] = MFMA32(xs, qf[g_ & 1][jt], num[jt]);
;                     __builtin_amdgcn_sched_barrier(0);
;                     if (s2 == 1) asm volatile("" : "+v"(num[0]), "+v"(num[1]), "+v"(num[2]), "+v"(num[3]) :: "memory"); }
;             }
; #pragma unroll
;             for (int jt = 0; jt < 4; ++jt) { const float ws_ = sWST[32 * jt + r];
; #pragma unroll
;                 for (int e = 0; e < 16; ++e) num[jt][e] *= ws_; }
;             __syncthreads();
	v_mfma_f32_32x32x16_bf16 v[64:79], v[238:241], v[218:221], v[64:79]
	v_mfma_f32_32x32x16_bf16 v[112:127], v[238:241], v[206:209], v[112:127]
	ds_read2_b64 v[206:209], v195 offset0:12 offset1:14
	ds_read2_b64 v[210:213], v196 offset0:76 offset1:78
	ds_read2_b64 v[214:217], v197 offset0:140 offset1:142
	ds_read2_b64 v[218:221], v242 offset0:204 offset1:206
	v_cvt_pk_bf16_f32 v238, v16, v17
	v_cvt_pk_bf16_f32 v239, v18, v19
	v_cvt_pk_bf16_f32 v240, v20, v21
	v_cvt_pk_bf16_f32 v241, v22, v23
	s_waitcnt lgkmcnt(6)
	s_nop 0
	v_mfma_f32_32x32x16_bf16 v[96:111], v[238:241], v[226:229], v[96:111]
	s_waitcnt lgkmcnt(5)
	v_mfma_f32_32x32x16_bf16 v[80:95], v[238:241], v[230:233], v[80:95]
	s_waitcnt lgkmcnt(4)
	v_mfma_f32_32x32x16_bf16 v[64:79], v[238:241], v[234:237], v[64:79]
	v_mfma_f32_32x32x16_bf16 v[112:127], v[238:241], v[222:225], v[112:127]
	ds_read2_b64 v[222:225], v195 offset0:16 offset1:18
	ds_read2_b64 v[226:229], v196 offset0:80 offset1:82
	ds_read2_b64 v[230:233], v197 offset0:144 offset1:146
	ds_read2_b64 v[234:237], v242 offset0:208 offset1:210
	v_cvt_pk_bf16_f32 v238, v24, v25
	v_cvt_pk_bf16_f32 v239, v26, v27
	v_cvt_pk_bf16_f32 v240, v28, v29
	v_cvt_pk_bf16_f32 v241, v30, v31
	s_waitcnt lgkmcnt(6)
	s_nop 0
	v_mfma_f32_32x32x16_bf16 v[96:111], v[238:241], v[210:213], v[96:111]
	s_waitcnt lgkmcnt(5)
	v_mfma_f32_32x32x16_bf16 v[80:95], v[238:241], v[214:217], v[80:95]
	s_waitcnt lgkmcnt(4)
	v_mfma_f32_32x32x16_bf16 v[64:79], v[238:241], v[218:221], v[64:79]
	v_mfma_f32_32x32x16_bf16 v[112:127], v[238:241], v[206:209], v[112:127]
	ds_read2_b64 v[206:209], v195 offset0:20 offset1:22
	ds_read2_b64 v[210:213], v196 offset0:84 offset1:86
	ds_read2_b64 v[214:217], v197 offset0:148 offset1:150
	ds_read2_b64 v[218:221], v242 offset0:212 offset1:214
	v_cvt_pk_bf16_f32 v238, v32, v33
	v_cvt_pk_bf16_f32 v239, v34, v35
	v_cvt_pk_bf16_f32 v240, v36, v37
	v_cvt_pk_bf16_f32 v241, v38, v39
	s_waitcnt lgkmcnt(6)
	s_nop 0
	v_mfma_f32_32x32x16_bf16 v[96:111], v[238:241], v[226:229], v[96:111]
	s_waitcnt lgkmcnt(5)
	v_mfma_f32_32x32x16_bf16 v[80:95], v[238:241], v[230:233], v[80:95]
	s_waitcnt lgkmcnt(4)
	v_mfma_f32_32x32x16_bf16 v[64:79], v[238:241], v[234:237], v[64:79]
	v_mfma_f32_32x32x16_bf16 v[112:127], v[238:241], v[222:225], v[112:127]
	ds_read2_b64 v[222:225], v195 offset0:24 offset1:26
	ds_read2_b64 v[226:229], v196 offset0:88 offset1:90
	ds_read2_b64 v[230:233], v197 offset0:152 offset1:154
	ds_read2_b64 v[234:237], v242 offset0:216 offset1:218
	v_cvt_pk_bf16_f32 v238, v40, v41
	v_cvt_pk_bf16_f32 v239, v42, v43
	v_cvt_pk_bf16_f32 v240, v44, v45
	v_cvt_pk_bf16_f32 v241, v46, v47
	s_waitcnt lgkmcnt(6)
	s_nop 0
	v_mfma_f32_32x32x16_bf16 v[96:111], v[238:241], v[210:213], v[96:111]
	s_waitcnt lgkmcnt(5)
	v_mfma_f32_32x32x16_bf16 v[80:95], v[238:241], v[214:217], v[80:95]
	s_waitcnt lgkmcnt(4)
	v_mfma_f32_32x32x16_bf16 v[64:79], v[238:241], v[218:221], v[64:79]
	v_mfma_f32_32x32x16_bf16 v[112:127], v[238:241], v[206:209], v[112:127]
	ds_read2_b64 v[206:209], v195 offset0:28 offset1:30
	ds_read2_b64 v[210:213], v196 offset0:92 offset1:94
	ds_read2_b64 v[214:217], v197 offset0:156 offset1:158
	ds_read2_b64 v[218:221], v242 offset0:220 offset1:222
	v_cvt_pk_bf16_f32 v238, v48, v49
	v_cvt_pk_bf16_f32 v239, v50, v51
	v_cvt_pk_bf16_f32 v240, v52, v53
	v_cvt_pk_bf16_f32 v241, v54, v55
	s_waitcnt lgkmcnt(6)
	s_nop 0
	v_mfma_f32_32x32x16_bf16 v[96:111], v[238:241], v[226:229], v[96:111]
	s_waitcnt lgkmcnt(5)
	v_mfma_f32_32x32x16_bf16 v[80:95], v[238:241], v[230:233], v[80:95]
	s_waitcnt lgkmcnt(4)
	v_mfma_f32_32x32x16_bf16 v[64:79], v[238:241], v[234:237], v[64:79]
	v_mfma_f32_32x32x16_bf16 v[112:127], v[238:241], v[222:225], v[112:127]
	v_cvt_pk_bf16_f32 v222, v56, v57
	v_cvt_pk_bf16_f32 v223, v58, v59
	v_cvt_pk_bf16_f32 v224, v60, v61
	v_cvt_pk_bf16_f32 v225, v62, v63
	s_waitcnt lgkmcnt(2)
	s_nop 0
	v_mfma_f32_32x32x16_bf16 v[96:111], v[222:225], v[210:213], v[96:111]
	s_waitcnt lgkmcnt(1)
	v_mfma_f32_32x32x16_bf16 v[80:95], v[222:225], v[214:217], v[80:95]
	s_waitcnt lgkmcnt(0)
	v_mfma_f32_32x32x16_bf16 v[64:79], v[222:225], v[218:221], v[64:79]
	v_mfma_f32_32x32x16_bf16 v[112:127], v[222:225], v[206:209], v[112:127]
	s_add_i32 s2, 0, 0x19c00
	v_lshl_add_u32 v195, v192, 2, s2
	ds_read2_b32 v[196:197], v195 offset1:32
	s_add_i32 s3, 0, 0x11000
	s_waitcnt lgkmcnt(0)
	s_nop 6
	v_pk_mul_f32 v[126:127], v[196:197], v[126:127] op_sel_hi:[0,1]
	v_pk_mul_f32 v[124:125], v[196:197], v[124:125] op_sel_hi:[0,1]
	v_pk_mul_f32 v[122:123], v[196:197], v[122:123] op_sel_hi:[0,1]
	v_pk_mul_f32 v[120:121], v[196:197], v[120:121] op_sel_hi:[0,1]
	v_pk_mul_f32 v[118:119], v[196:197], v[118:119] op_sel_hi:[0,1]
	v_pk_mul_f32 v[116:117], v[196:197], v[116:117] op_sel_hi:[0,1]
	v_pk_mul_f32 v[114:115], v[196:197], v[114:115] op_sel_hi:[0,1]
	v_pk_mul_f32 v[112:113], v[196:197], v[112:113] op_sel_hi:[0,1]
	v_mov_b32_e32 v192, v197
	ds_read2_b32 v[196:197], v195 offset0:64 offset1:96
	v_pk_mul_f32 v[110:111], v[192:193], v[110:111] op_sel_hi:[0,1]
	v_pk_mul_f32 v[108:109], v[192:193], v[108:109] op_sel_hi:[0,1]
	v_pk_mul_f32 v[106:107], v[192:193], v[106:107] op_sel_hi:[0,1]
	v_pk_mul_f32 v[104:105], v[192:193], v[104:105] op_sel_hi:[0,1]
	v_pk_mul_f32 v[102:103], v[192:193], v[102:103] op_sel_hi:[0,1]
	v_pk_mul_f32 v[100:101], v[192:193], v[100:101] op_sel_hi:[0,1]
	v_pk_mul_f32 v[98:99], v[192:193], v[98:99] op_sel_hi:[0,1]
	v_pk_mul_f32 v[96:97], v[192:193], v[96:97] op_sel_hi:[0,1]
	s_waitcnt lgkmcnt(0)
	v_mov_b32_e32 v192, v197
	v_pk_mul_f32 v[78:79], v[78:79], v[192:193] op_sel_hi:[1,0]
	v_pk_mul_f32 v[76:77], v[76:77], v[192:193] op_sel_hi:[1,0]
	v_pk_mul_f32 v[74:75], v[74:75], v[192:193] op_sel_hi:[1,0]
	v_pk_mul_f32 v[72:73], v[72:73], v[192:193] op_sel_hi:[1,0]
	v_pk_mul_f32 v[70:71], v[70:71], v[192:193] op_sel_hi:[1,0]
	v_pk_mul_f32 v[68:69], v[68:69], v[192:193] op_sel_hi:[1,0]
	v_pk_mul_f32 v[66:67], v[66:67], v[192:193] op_sel_hi:[1,0]
	v_pk_mul_f32 v[64:65], v[64:65], v[192:193] op_sel_hi:[1,0]
	s_barrier
; #define LAS __attribute__((address_space(3)))
; DI int lane_id() { int l; asm volatile("v_mbcnt_lo_u32_b32 %0, -1, 0\n\tv_mbcnt_hi_u32_b32 %0, -1, %0" : "=v"(l)); return l; }
; #define MFMA32(a, b, c) __builtin_amdgcn_mfma_f32_32x32x16_bf16((a), (b), (c), 0, 0, 0)
; template <bool PASS2, int DIRT>
; DI void mlstm_item(const Params& P, LAS unsigned char* lds, int st, int g) {
;     ...
;             tid = (wid << 6) | lane_id(); asm volatile("" : "+v"(tid)); lane = tid & 63; r = lane & 31; hh = lane >> 5;
;             {
;                 bf16x8 pf[2][4];
;                 auto ldp = [&](int ks, bf16x8 (&pb)[4]) {
; #pragma unroll
;                     for (int jt = 0; jt < 4; ++jt) { const bool on = dir ? (ks >= 2 * jt) : (ks <= 2 * jt + 1); if (on) pb[jt] = *(const LAS bf16x8*)(PS + off_b(32 * jt + r, 2 * ks + hh)); } };
;                 ldp(0, pf[0]);
; #pragma unroll
;                 for (int ks = 0; ks < 8; ++ks) {
;                     if (ks + 1 < 8) ldp(ks + 1, pf[(ks + 1) & 1]);
;                     __builtin_amdgcn_sched_barrier(0);
; #pragma unroll
;                     for (int jt = 0; jt < 4; ++jt) { const bool on = dir ? (ks >= 2 * jt) : (ks <= 2 * jt + 1); if (on) num[jt] = MFMA32(vf[ks], pf[ks & 1][jt], num[jt]); }
;                     __builtin_amdgcn_sched_barrier(0); }
;                 asm volatile("" : "+v"(num[0]), "+v"(num[1]), "+v"(num[2]), "+v"(num[3]) :: "memory");
;             }
;             bf16_t* Hd = (bf16_t*)(P.ws + (dir ? WS_HB : WS_HF));
; #pragma unroll
;             for (int jt = 0; jt < 4; ++jt) { const int j = 32 * jt + r;
;                 const float den = (sDENP[j] + sDENP[128 + j]) + (sDENP[256 + j] + sDENP[384 + j]) + sWST[j] * ((sQNP[j] + sQNP[128 + j]) + (sQNP[256 + j] + sQNP[384 + j]));
;                 const float inv = 1.0f / fmaxf(fabsf(den), sCL[j]);
	v_mbcnt_lo_u32_b32 v192, -1, 0
	v_mbcnt_hi_u32_b32 v192, -1, v192
	v_pk_mul_f32 v[94:95], v[94:95], v[196:197] op_sel_hi:[1,0]
	v_or_b32_e32 v192, s97, v192
	v_pk_mul_f32 v[92:93], v[92:93], v[196:197] op_sel_hi:[1,0]
	v_and_b32_e32 v195, 31, v192
	v_bfe_u32 v192, v192, 5, 1
	v_pk_mul_f32 v[90:91], v[90:91], v[196:197] op_sel_hi:[1,0]
	v_pk_mul_f32 v[88:89], v[88:89], v[196:197] op_sel_hi:[1,0]
	v_pk_mul_f32 v[86:87], v[86:87], v[196:197] op_sel_hi:[1,0]
	v_pk_mul_f32 v[84:85], v[84:85], v[196:197] op_sel_hi:[1,0]
	v_pk_mul_f32 v[82:83], v[82:83], v[196:197] op_sel_hi:[1,0]
	v_pk_mul_f32 v[80:81], v[80:81], v[196:197] op_sel_hi:[1,0]
	v_mul_u32_u24_e32 v196, 0x110, v195
	v_lshlrev_b32_e32 v197, 4, v192
	v_add3_u32 v196, s3, v197, v196
	ds_read_b128 v[206:209], v196 offset:8704
	ds_read_b128 v[210:213], v196 offset:17408
	ds_read_b128 v[214:217], v196 offset:26112
	ds_read_b128 v[218:221], v196
	ds_read_b128 v[222:225], v196 offset:32
	ds_read_b128 v[226:229], v196 offset:8736
	ds_read_b128 v[230:233], v196 offset:17440
	ds_read_b128 v[234:237], v196 offset:26144
	s_waitcnt vmcnt(7) lgkmcnt(7)
	v_mfma_f32_32x32x16_bf16 v[96:111], v[188:191], v[206:209], v[96:111]
	s_waitcnt lgkmcnt(6)
	v_mfma_f32_32x32x16_bf16 v[80:95], v[188:191], v[210:213], v[80:95]
	s_waitcnt lgkmcnt(5)
	v_mfma_f32_32x32x16_bf16 v[64:79], v[188:191], v[214:217], v[64:79]
	s_waitcnt lgkmcnt(4)
	v_mfma_f32_32x32x16_bf16 v[112:127], v[188:191], v[218:221], v[112:127]
	ds_read_b128 v[206:209], v196 offset:8768
	ds_read_b128 v[210:213], v196 offset:17472
	ds_read_b128 v[214:217], v196 offset:26176
	s_waitcnt vmcnt(6) lgkmcnt(5)
	v_mfma_f32_32x32x16_bf16 v[96:111], v[184:187], v[226:229], v[96:111]
	s_waitcnt lgkmcnt(4)
	v_mfma_f32_32x32x16_bf16 v[80:95], v[184:187], v[230:233], v[80:95]
	s_waitcnt lgkmcnt(3)
	v_mfma_f32_32x32x16_bf16 v[64:79], v[184:187], v[234:237], v[64:79]
	v_mfma_f32_32x32x16_bf16 v[112:127], v[184:187], v[222:225], v[112:127]
	ds_read_b128 v[218:221], v196 offset:8800
	ds_read_b128 v[222:225], v196 offset:17504
	ds_read_b128 v[226:229], v196 offset:26208
	s_waitcnt vmcnt(5) lgkmcnt(5)
	v_mfma_f32_32x32x16_bf16 v[96:111], v[180:183], v[206:209], v[96:111]
	s_waitcnt lgkmcnt(4)
	v_mfma_f32_32x32x16_bf16 v[80:95], v[180:183], v[210:213], v[80:95]
	s_waitcnt lgkmcnt(3)
	v_mfma_f32_32x32x16_bf16 v[64:79], v[180:183], v[214:217], v[64:79]
	ds_read_b128 v[206:209], v196 offset:17536
	ds_read_b128 v[210:213], v196 offset:26240
	s_waitcnt vmcnt(4) lgkmcnt(4)
	v_mfma_f32_32x32x16_bf16 v[96:111], v[176:179], v[218:221], v[96:111]
	s_waitcnt lgkmcnt(3)
	v_mfma_f32_32x32x16_bf16 v[80:95], v[176:179], v[222:225], v[80:95]
	s_waitcnt lgkmcnt(2)
	v_mfma_f32_32x32x16_bf16 v[64:79], v[176:179], v[226:229], v[64:79]
	ds_read_b128 v[214:217], v196 offset:17568
	ds_read_b128 v[218:221], v196 offset:26272
	s_waitcnt vmcnt(3) lgkmcnt(3)
	v_mfma_f32_32x32x16_bf16 v[80:95], v[172:175], v[206:209], v[80:95]
	s_waitcnt lgkmcnt(2)
	v_mfma_f32_32x32x16_bf16 v[64:79], v[172:175], v[210:213], v[64:79]
	ds_read_b128 v[206:209], v196 offset:26304
	s_waitcnt vmcnt(2) lgkmcnt(2)
	v_mfma_f32_32x32x16_bf16 v[80:95], v[168:171], v[214:217], v[80:95]
	s_waitcnt lgkmcnt(1)
	v_mfma_f32_32x32x16_bf16 v[64:79], v[168:171], v[218:221], v[64:79]
	ds_read_b128 v[210:213], v196 offset:26336
	s_waitcnt vmcnt(1) lgkmcnt(1)
	v_mfma_f32_32x32x16_bf16 v[64:79], v[164:167], v[206:209], v[64:79]
	s_waitcnt vmcnt(0) lgkmcnt(0)
	v_mfma_f32_32x32x16_bf16 v[64:79], v[160:163], v[210:213], v[64:79]
	v_lshlrev_b32_e32 v192, 3, v192
	s_add_i32 s3, 0, 0x1a800
	v_lshlrev_b32_e32 v206, 2, v195
	v_lshl_add_u64 v[196:197], s[14:15], 0, v[192:193]
	v_add_u32_e32 v192, s3, v206
	ds_read_b32 v208, v192
	v_or_b32_e32 v192, 0x200, v206
	v_add_u32_e32 v207, s3, v192
	v_add_u32_e32 v192, s95, v192
	ds_read_b32 v210, v207
	ds_read_b32 v211, v192
	v_or_b32_e32 v207, 0x400, v206
	v_add_u32_e32 v209, s3, v207
	v_or_b32_e32 v215, 0x600, v206
	v_add_u32_e32 v192, s95, v207
	ds_read_b32 v212, v209
	ds_read_b32 v213, v192
	v_add_u32_e32 v209, s3, v215
	v_add_u32_e32 v192, s95, v215
	s_add_i32 s4, 0, 0x19e00
	ds_read_b32 v214, v209
	ds_read_b32 v215, v192
	v_add_u32_e32 v209, s2, v206
	v_add_u32_e32 v192, s4, v206
	ds_read_b32 v216, v209
	ds_read_b32 v192, v192
	v_add_u32_e32 v209, s95, v206
	ds_read_b32 v209, v209
	s_waitcnt lgkmcnt(1)
	v_max_f32_e32 v192, v192, v192
	s_waitcnt lgkmcnt(0)
; DI unsigned pk2(float a, float b) { f32x2 f = {a, b}; bf16x2_t h = __builtin_convertvector(f, bf16x2_t); return __builtin_bit_cast(unsigned, h); }
; template <bool PASS2, int DIRT>
; DI void mlstm_item(const Params& P, LAS unsigned char* lds, int st, int g) {
;     ...
;             for (int jt = 0; jt < 4; ++jt) { const int j = 32 * jt + r;
;                 const float den = (sDENP[j] + sDENP[128 + j]) + (sDENP[256 + j] + sDENP[384 + j]) + sWST[j] * ((sQNP[j] + sQNP[128 + j]) + (sQNP[256 + j] + sQNP[384 + j]));
;                 const float inv = 1.0f / fmaxf(fabsf(den), sCL[j]);
;                 bf16_t* hp = Hd + (size_t)(tok0 + j) * 1024 + h * 256 + 32 * wid + 4 * hh;
; #pragma unroll
;                 for (int gq = 0; gq < 4; ++gq) { u32x2 w; w.x = pk2(num[jt][4 * gq] * inv, num[jt][4 * gq + 1] * inv); w.y = pk2(num[jt][4 * gq + 2] * inv, num[jt][4 * gq + 3] * inv); *(u32x2*)(hp + 8 * gq) = w; } }
	v_pk_add_f32 v[208:209], v[208:209], v[210:211]
	v_pk_add_f32 v[210:211], v[212:213], v[214:215]
	s_nop 0
	v_pk_add_f32 v[208:209], v[208:209], v[210:211]
	s_nop 0
	v_fmac_f32_e32 v208, v216, v209
	v_max_f32_e64 v192, |v208|, v192
	v_div_scale_f32 v207, s[44:45], v192, v192, 1.0
	v_rcp_f32_e32 v208, v207
	s_nop 0
	v_fma_f32 v209, -v207, v208, 1.0
	v_fmac_f32_e32 v208, v209, v208
	v_div_scale_f32 v209, vcc, 1.0, v192, 1.0
	v_mul_f32_e32 v210, v209, v208
	v_fma_f32 v211, -v207, v210, v209
	v_fmac_f32_e32 v210, v211, v208
	v_fma_f32 v207, -v207, v210, v209
	v_div_fmas_f32 v207, v207, v208, v210
	v_div_fixup_f32 v208, v207, v192, 1.0
	v_or_b32_e32 v192, s67, v195
	v_lshlrev_b32_e32 v192, 11, v192
	v_pk_mul_f32 v[112:113], v[112:113], v[208:209] op_sel_hi:[1,0]
	v_pk_mul_f32 v[114:115], v[114:115], v[208:209] op_sel_hi:[1,0]
	v_lshl_add_u64 v[210:211], v[196:197], 0, v[192:193]
	v_cvt_pk_bf16_f32 v244, v112, v113
	v_cvt_pk_bf16_f32 v245, v114, v115
	v_pk_mul_f32 v[112:113], v[116:117], v[208:209] op_sel_hi:[1,0]
	v_pk_mul_f32 v[114:115], v[118:119], v[208:209] op_sel_hi:[1,0]
	v_cvt_pk_bf16_f32 v248, v112, v113
	v_cvt_pk_bf16_f32 v249, v114, v115
	v_pk_mul_f32 v[112:113], v[120:121], v[208:209] op_sel_hi:[1,0]
	v_pk_mul_f32 v[114:115], v[122:123], v[208:209] op_sel_hi:[1,0]
	v_cvt_pk_bf16_f32 v246, v112, v113
	v_cvt_pk_bf16_f32 v247, v114, v115
	v_pk_mul_f32 v[112:113], v[124:125], v[208:209] op_sel_hi:[1,0]
	v_pk_mul_f32 v[114:115], v[126:127], v[208:209] op_sel_hi:[1,0]
	v_or_b32_e32 v120, 32, v195
	v_cvt_pk_bf16_f32 v250, v112, v113
	v_cvt_pk_bf16_f32 v251, v114, v115
	v_lshlrev_b32_e32 v121, 2, v120
	v_or_b32_e32 v115, 0x280, v206
	v_mbcnt_lo_u32_b32 v252, -1, 0
	v_mbcnt_hi_u32_b32 v252, -1, v252
	v_lshrrev_b32_e32 v252, 5, v252
	v_mul_u32_u24_e32 v252, 24, v252
	v_mov_b32_e32 v253, 0
	v_permlane32_swap_b32_e32 v244, v246
	v_permlane32_swap_b32_e32 v245, v247
	v_permlane32_swap_b32_e32 v248, v250
	v_permlane32_swap_b32_e32 v249, v251
	v_lshl_add_u64 v[252:253], v[210:211], 0, v[252:253]
	global_store_dwordx4 v[252:253], v[244:247], off
	global_store_dwordx4 v[252:253], v[248:251], off offset:16
	v_add_u32_e32 v112, s3, v121
	v_add_u32_e32 v113, s3, v115
	v_or_b32_e32 v117, 0x480, v206
	v_add_u32_e32 v115, s95, v115
	ds_read_b32 v112, v112
	ds_read_b32 v114, v113
	ds_read_b32 v115, v115
	v_add_u32_e32 v113, s3, v117
	v_or_b32_e32 v119, 0x680, v206
	v_add_u32_e32 v117, s95, v117
	ds_read_b32 v116, v113
	ds_read_b32 v117, v117
	v_add_u32_e32 v113, s3, v119
	v_add_u32_e32 v119, s95, v119
	ds_read_b32 v118, v113
	ds_read_b32 v119, v119
	v_add_u32_e32 v113, s2, v121
	ds_read_b32 v122, v113
	v_add_u32_e32 v113, s95, v121
	ds_read_b32 v113, v113
	s_waitcnt lgkmcnt(0)
	v_pk_add_f32 v[112:113], v[112:113], v[114:115]
	v_pk_add_f32 v[114:115], v[116:117], v[118:119]
	s_nop 0
	v_pk_add_f32 v[112:113], v[112:113], v[114:115]
	s_nop 0
	v_fmac_f32_e32 v112, v122, v113
	v_add_u32_e32 v113, s4, v121
	ds_read_b32 v113, v113
	s_waitcnt lgkmcnt(0)
	v_max_f32_e32 v113, v113, v113
	v_max_f32_e64 v112, |v112|, v113
	v_div_scale_f32 v113, s[44:45], v112, v112, 1.0
	v_rcp_f32_e32 v114, v113
	s_nop 0
	v_fma_f32 v115, -v113, v114, 1.0
	v_fmac_f32_e32 v114, v115, v114
	v_div_scale_f32 v115, vcc, 1.0, v112, 1.0
	v_mul_f32_e32 v116, v115, v114
	v_fma_f32 v117, -v113, v116, v115
	v_fmac_f32_e32 v116, v117, v114
	v_fma_f32 v113, -v113, v116, v115
	v_div_fmas_f32 v113, v113, v114, v116
	v_div_fixup_f32 v112, v113, v112, 1.0
	v_or_b32_e32 v113, s67, v120
	v_lshlrev_b32_e32 v192, 11, v113
	v_pk_mul_f32 v[96:97], v[96:97], v[112:113] op_sel_hi:[1,0]
	v_pk_mul_f32 v[98:99], v[98:99], v[112:113] op_sel_hi:[1,0]
	v_lshl_add_u64 v[114:115], v[196:197], 0, v[192:193]
	v_cvt_pk_bf16_f32 v244, v96, v97
	v_cvt_pk_bf16_f32 v245, v98, v99
	v_pk_mul_f32 v[96:97], v[100:101], v[112:113] op_sel_hi:[1,0]
	v_pk_mul_f32 v[98:99], v[102:103], v[112:113] op_sel_hi:[1,0]
	v_cvt_pk_bf16_f32 v248, v96, v97
	v_cvt_pk_bf16_f32 v249, v98, v99
	v_pk_mul_f32 v[96:97], v[104:105], v[112:113] op_sel_hi:[1,0]
	v_pk_mul_f32 v[98:99], v[106:107], v[112:113] op_sel_hi:[1,0]
	v_cvt_pk_bf16_f32 v246, v96, v97
	v_cvt_pk_bf16_f32 v247, v98, v99
	v_pk_mul_f32 v[96:97], v[108:109], v[112:113] op_sel_hi:[1,0]
	v_pk_mul_f32 v[98:99], v[110:111], v[112:113] op_sel_hi:[1,0]
	v_or_b32_e32 v104, 64, v195
	v_cvt_pk_bf16_f32 v250, v96, v97
	v_cvt_pk_bf16_f32 v251, v98, v99
	v_lshlrev_b32_e32 v105, 2, v104
	v_or_b32_e32 v99, 0x300, v206
	v_mbcnt_lo_u32_b32 v252, -1, 0
	v_mbcnt_hi_u32_b32 v252, -1, v252
	v_lshrrev_b32_e32 v252, 5, v252
	v_mul_u32_u24_e32 v252, 24, v252
	v_mov_b32_e32 v253, 0
	v_permlane32_swap_b32_e32 v244, v246
	v_permlane32_swap_b32_e32 v245, v247
	v_permlane32_swap_b32_e32 v248, v250
	v_permlane32_swap_b32_e32 v249, v251
	v_lshl_add_u64 v[252:253], v[114:115], 0, v[252:253]
	global_store_dwordx4 v[252:253], v[244:247], off
	global_store_dwordx4 v[252:253], v[248:251], off offset:16
	v_add_u32_e32 v96, s3, v105
	v_add_u32_e32 v97, s3, v99
	v_or_b32_e32 v101, 0x500, v206
	v_add_u32_e32 v99, s95, v99
	ds_read_b32 v96, v96
	ds_read_b32 v98, v97
	ds_read_b32 v99, v99
	v_add_u32_e32 v97, s3, v101
	v_or_b32_e32 v103, 0x700, v206
	v_add_u32_e32 v101, s95, v101
	ds_read_b32 v100, v97
	ds_read_b32 v101, v101
	v_add_u32_e32 v97, s3, v103
	v_add_u32_e32 v103, s95, v103
	ds_read_b32 v102, v97
	ds_read_b32 v103, v103
	v_add_u32_e32 v97, s2, v105
	ds_read_b32 v106, v97
	v_add_u32_e32 v97, s95, v105
	ds_read_b32 v97, v97
	s_waitcnt lgkmcnt(0)
	v_pk_add_f32 v[96:97], v[96:97], v[98:99]
	v_pk_add_f32 v[98:99], v[100:101], v[102:103]
	s_nop 0
	v_pk_add_f32 v[96:97], v[96:97], v[98:99]
	s_nop 0
	v_fmac_f32_e32 v96, v106, v97
	v_add_u32_e32 v97, s4, v105
	ds_read_b32 v97, v97
	s_waitcnt lgkmcnt(0)
; DI unsigned pk2(float a, float b) { f32x2 f = {a, b}; bf16x2_t h = __builtin_convertvector(f, bf16x2_t); return __builtin_bit_cast(unsigned, h); }
; template <bool PASS2, int DIRT>
; DI void mlstm_item(const Params& P, LAS unsigned char* lds, int st, int g) {
;     ...
;             for (int jt = 0; jt < 4; ++jt) { const int j = 32 * jt + r;
;                 const float den = (sDENP[j] + sDENP[128 + j]) + (sDENP[256 + j] + sDENP[384 + j]) + sWST[j] * ((sQNP[j] + sQNP[128 + j]) + (sQNP[256 + j] + sQNP[384 + j]));
;                 const float inv = 1.0f / fmaxf(fabsf(den), sCL[j]);
;                 bf16_t* hp = Hd + (size_t)(tok0 + j) * 1024 + h * 256 + 32 * wid + 4 * hh;
; #pragma unroll
;                 for (int gq = 0; gq < 4; ++gq) { u32x2 w; w.x = pk2(num[jt][4 * gq] * inv, num[jt][4 * gq + 1] * inv); w.y = pk2(num[jt][4 * gq + 2] * inv, num[jt][4 * gq + 3] * inv); *(u32x2*)(hp + 8 * gq) = w; } }
;     ...
;         if (ci + 1 < nchunks) { const int tokn = chunk_tok0(ci + 1);
; #pragma unroll
;             for (int i = 0; i < 4; ++i) { const int n = tid + 512 * i, row = n >> 4, ch = n & 15; kq[i] = *(const u32x4*)(Kg + (size_t)(tokn + row) * 512 + h * 128 + ch * 8);
;                 if (PASS2) kq[4 + i] = *(const u32x4*)(Qg + (size_t)(tokn + row) * 512 + h * 128 + ch * 8); } }
	v_max_f32_e32 v97, v97, v97
	v_max_f32_e64 v96, |v96|, v97
	v_div_scale_f32 v97, s[44:45], v96, v96, 1.0
	v_rcp_f32_e32 v98, v97
	s_nop 0
	v_fma_f32 v99, -v97, v98, 1.0
	v_fmac_f32_e32 v98, v99, v98
	v_div_scale_f32 v99, vcc, 1.0, v96, 1.0
	v_mul_f32_e32 v100, v99, v98
	v_fma_f32 v101, -v97, v100, v99
	v_fmac_f32_e32 v100, v101, v98
	v_fma_f32 v97, -v97, v100, v99
	v_div_fmas_f32 v97, v97, v98, v100
	v_div_fixup_f32 v96, v97, v96, 1.0
	v_or_b32_e32 v97, s67, v104
	v_lshlrev_b32_e32 v192, 11, v97
	v_pk_mul_f32 v[80:81], v[80:81], v[96:97] op_sel_hi:[1,0]
	v_pk_mul_f32 v[82:83], v[82:83], v[96:97] op_sel_hi:[1,0]
	v_lshl_add_u64 v[98:99], v[196:197], 0, v[192:193]
	v_cvt_pk_bf16_f32 v244, v80, v81
	v_cvt_pk_bf16_f32 v245, v82, v83
	v_pk_mul_f32 v[80:81], v[84:85], v[96:97] op_sel_hi:[1,0]
	v_pk_mul_f32 v[82:83], v[86:87], v[96:97] op_sel_hi:[1,0]
	v_cvt_pk_bf16_f32 v248, v80, v81
	v_cvt_pk_bf16_f32 v249, v82, v83
	v_pk_mul_f32 v[80:81], v[88:89], v[96:97] op_sel_hi:[1,0]
	v_pk_mul_f32 v[82:83], v[90:91], v[96:97] op_sel_hi:[1,0]
	v_cvt_pk_bf16_f32 v246, v80, v81
	v_cvt_pk_bf16_f32 v247, v82, v83
	v_pk_mul_f32 v[80:81], v[92:93], v[96:97] op_sel_hi:[1,0]
	v_pk_mul_f32 v[82:83], v[94:95], v[96:97] op_sel_hi:[1,0]
	v_or_b32_e32 v88, 0x60, v195
	v_cvt_pk_bf16_f32 v250, v80, v81
	v_cvt_pk_bf16_f32 v251, v82, v83
	v_lshlrev_b32_e32 v89, 2, v88
	v_or_b32_e32 v83, 0x380, v206
	v_mbcnt_lo_u32_b32 v252, -1, 0
	v_mbcnt_hi_u32_b32 v252, -1, v252
	v_lshrrev_b32_e32 v252, 5, v252
	v_mul_u32_u24_e32 v252, 24, v252
	v_mov_b32_e32 v253, 0
	v_permlane32_swap_b32_e32 v244, v246
	v_permlane32_swap_b32_e32 v245, v247
	v_permlane32_swap_b32_e32 v248, v250
	v_permlane32_swap_b32_e32 v249, v251
	v_lshl_add_u64 v[252:253], v[98:99], 0, v[252:253]
	global_store_dwordx4 v[252:253], v[244:247], off
	global_store_dwordx4 v[252:253], v[248:251], off offset:16
	v_add_u32_e32 v80, s3, v89
	v_add_u32_e32 v81, s3, v83
	v_or_b32_e32 v85, 0x580, v206
	v_add_u32_e32 v83, s95, v83
	ds_read_b32 v80, v80
	ds_read_b32 v82, v81
	ds_read_b32 v83, v83
	v_add_u32_e32 v81, s3, v85
	v_or_b32_e32 v87, 0x780, v206
	v_add_u32_e32 v85, s95, v85
	ds_read_b32 v84, v81
	ds_read_b32 v85, v85
	v_add_u32_e32 v81, s3, v87
	v_add_u32_e32 v87, s95, v87
	ds_read_b32 v86, v81
	ds_read_b32 v87, v87
	v_add_u32_e32 v81, s2, v89
	ds_read_b32 v90, v81
	v_add_u32_e32 v81, s95, v89
	ds_read_b32 v81, v81
	s_waitcnt lgkmcnt(0)
	v_pk_add_f32 v[80:81], v[80:81], v[82:83]
	v_pk_add_f32 v[82:83], v[84:85], v[86:87]
	s_nop 0
	v_pk_add_f32 v[80:81], v[80:81], v[82:83]
	s_nop 0
	v_fmac_f32_e32 v80, v90, v81
	v_add_u32_e32 v81, s4, v89
	ds_read_b32 v81, v81
	s_add_i32 s4, s72, 1
	s_cmp_lg_u32 s72, 7
	s_waitcnt lgkmcnt(0)
	v_max_f32_e32 v81, v81, v81
	v_max_f32_e64 v80, |v80|, v81
	v_div_scale_f32 v81, s[2:3], v80, v80, 1.0
	v_rcp_f32_e32 v82, v81
	s_mov_b64 s[2:3], -1
	v_fma_f32 v83, -v81, v82, 1.0
	v_fmac_f32_e32 v82, v83, v82
	v_div_scale_f32 v83, vcc, 1.0, v80, 1.0
	v_mul_f32_e32 v84, v83, v82
	v_fma_f32 v85, -v81, v84, v83
	v_fmac_f32_e32 v84, v85, v82
	v_fma_f32 v81, -v81, v84, v83
	v_div_fmas_f32 v81, v81, v82, v84
	v_div_fixup_f32 v80, v81, v80, 1.0
	v_or_b32_e32 v81, s67, v88
	v_lshlrev_b32_e32 v192, 11, v81
	v_pk_mul_f32 v[64:65], v[64:65], v[80:81] op_sel_hi:[1,0]
	v_pk_mul_f32 v[66:67], v[66:67], v[80:81] op_sel_hi:[1,0]
	v_lshl_add_u64 v[82:83], v[196:197], 0, v[192:193]
	v_cvt_pk_bf16_f32 v244, v64, v65
	v_cvt_pk_bf16_f32 v245, v66, v67
	v_pk_mul_f32 v[64:65], v[68:69], v[80:81] op_sel_hi:[1,0]
	v_pk_mul_f32 v[66:67], v[70:71], v[80:81] op_sel_hi:[1,0]
	v_cvt_pk_bf16_f32 v248, v64, v65
	v_cvt_pk_bf16_f32 v249, v66, v67
	v_pk_mul_f32 v[64:65], v[72:73], v[80:81] op_sel_hi:[1,0]
	v_pk_mul_f32 v[66:67], v[74:75], v[80:81] op_sel_hi:[1,0]
	v_cvt_pk_bf16_f32 v246, v64, v65
	v_cvt_pk_bf16_f32 v247, v66, v67
	v_pk_mul_f32 v[64:65], v[76:77], v[80:81] op_sel_hi:[1,0]
	v_pk_mul_f32 v[66:67], v[78:79], v[80:81] op_sel_hi:[1,0]
	v_cvt_pk_bf16_f32 v250, v64, v65
	v_cvt_pk_bf16_f32 v251, v66, v67
	v_mbcnt_lo_u32_b32 v252, -1, 0
	v_mbcnt_hi_u32_b32 v252, -1, v252
	v_lshrrev_b32_e32 v252, 5, v252
	v_mul_u32_u24_e32 v252, 24, v252
	v_mov_b32_e32 v253, 0
	v_permlane32_swap_b32_e32 v244, v246
	v_permlane32_swap_b32_e32 v245, v247
	v_permlane32_swap_b32_e32 v248, v250
	v_permlane32_swap_b32_e32 v249, v251
	v_lshl_add_u64 v[252:253], v[82:83], 0, v[252:253]
	global_store_dwordx4 v[252:253], v[244:247], off
	global_store_dwordx4 v[252:253], v[248:251], off offset:16
	v_mbcnt_lo_u32_b32 v64, -1, 0
	v_mbcnt_hi_u32_b32 v64, -1, v64
	s_nop 0
	v_or_b32_e32 v97, s97, v64
	s_nop 0
	v_lshlrev_b32_e32 v96, 3, v97
	s_cbranch_scc0 .LBB0_812
	s_lshl_b32 s2, s4, 7
	v_lshlrev_b32_e32 v64, 4, v97
	v_add_u32_e32 v72, 0x200, v97
	v_add_u32_e32 v80, 0x400, v97
	v_add_u32_e32 v92, 0x600, v97
	s_add_i32 s2, s2, s43
	v_and_b32_e32 v192, 0xf0, v64
	v_ashrrev_i32_e32 v64, 4, v97
	v_ashrrev_i32_e32 v72, 4, v72
	v_ashrrev_i32_e32 v80, 4, v80
	v_ashrrev_i32_e32 v92, 4, v92
	v_add_u32_e32 v64, s2, v64
	v_add_u32_e32 v72, s2, v72
	v_add_u32_e32 v80, s2, v80
	v_add_u32_e32 v92, s2, v92
	v_ashrrev_i32_e32 v65, 31, v64
	v_ashrrev_i32_e32 v73, 31, v72
	v_ashrrev_i32_e32 v81, 31, v80
	v_ashrrev_i32_e32 v93, 31, v92
	v_lshl_add_u64 v[88:89], s[6:7], 0, v[192:193]
	v_lshl_add_u64 v[90:91], s[8:9], 0, v[192:193]
	v_lshlrev_b64 v[64:65], 10, v[64:65]
	v_lshlrev_b64 v[72:73], 10, v[72:73]
	v_lshlrev_b64 v[80:81], 10, v[80:81]
	v_lshlrev_b64 v[92:93], 10, v[92:93]
	v_lshl_add_u64 v[66:67], v[88:89], 0, v[64:65]
	v_lshl_add_u64 v[64:65], v[90:91], 0, v[64:65]
	v_lshl_add_u64 v[74:75], v[88:89], 0, v[72:73]
	v_lshl_add_u64 v[72:73], v[90:91], 0, v[72:73]
	v_lshl_add_u64 v[82:83], v[88:89], 0, v[80:81]
	v_lshl_add_u64 v[80:81], v[90:91], 0, v[80:81]
	v_lshl_add_u64 v[88:89], v[88:89], 0, v[92:93]
	v_lshl_add_u64 v[90:91], v[90:91], 0, v[92:93]
	global_load_dwordx4 v[128:131], v[66:67], off
	s_nop 0
	global_load_dwordx4 v[132:135], v[64:65], off
	s_nop 0
	global_load_dwordx4 v[136:139], v[74:75], off
	s_nop 0
	global_load_dwordx4 v[140:143], v[72:73], off
	s_nop 0
	global_load_dwordx4 v[144:147], v[82:83], off
	s_nop 0
	global_load_dwordx4 v[148:151], v[80:81], off
	s_nop 0
	global_load_dwordx4 v[152:155], v[88:89], off
	s_nop 0
	global_load_dwordx4 v[156:159], v[90:91], off
	v_lshlrev_b32_e32 v98, 3, v97
	s_mov_b64 s[2:3], 0
